# v42 + one sc1 dummy load per wave (issued after last x-row group) prefetching the G32/P32 tables into L2 ahead of tier-1/output gather
# speedup vs baseline: 1.0060x; 1.0060x over previous
.LBB1_6:
	s_or_b64 exec, exec, s[4:5]
	v_mov_b32_e32 v6, 0x18010
	v_mov_b32_e32 v2, 0x18000
	s_waitcnt lgkmcnt(0)
	s_barrier
	s_load_dword s98, s[12:13], 0x0
	s_waitcnt vmcnt(14)
	ds_read_b128 v[2:5], v2
	ds_read_b128 v[6:9], v6
	s_load_dwordx4 s[36:39], s[0:1], 0x20
	s_movk_i32 s0, 0x2000
	v_lshrrev_b32_e32 v125, 4, v131
	s_waitcnt lgkmcnt(0)
	v_mov_b32_e32 v14, v2
	v_mov_b32_e32 v15, v6
	v_mov_b32_e32 v6, v3
	v_pk_add_f32 v[2:3], v[14:15], v[6:7]
	v_mov_b32_e32 v6, v4
	v_mov_b32_e32 v7, v8
	v_mov_b32_e32 v8, v5
	v_pk_add_f32 v[4:5], v[6:7], v[8:9]
	v_mov_b32_e32 v14, 0x18060
	v_pk_add_f32 v[2:3], v[2:3], v[4:5]
	v_add_co_u32_e32 v42, vcc, s0, v82
	v_add_f32_e32 v2, v2, v3
	v_mul_f32_e32 v132, 0x3a800000, v2
	v_and_b32_e32 v107, 15, v0
	v_mov_b32_e32 v2, 0x18020
	v_mov_b32_e32 v3, 0x18030
	v_lshl_add_u32 v13, v13, 2, v14
	v_pk_add_f32 v[10:11], v[10:11], v[132:133] op_sel_hi:[1,0] neg_lo:[0,1] neg_hi:[0,1]
	v_lshlrev_b32_e32 v85, 13, v1
	v_xor_b32_e32 v114, v125, v0
	v_addc_co_u32_e32 v43, vcc, 0, v83, vcc
	s_movk_i32 s0, 0x3000
	ds_read_b128 v[6:9], v2
	ds_read_b128 v[2:5], v3
	ds_write_b64 v13, v[10:11]
	v_lshl_or_b32 v84, v107, 9, v85
	v_lshlrev_b32_e32 v10, 4, v114
	s_movk_i32 s41, 0xf0
	v_add_co_u32_e32 v44, vcc, s0, v82
	v_lshlrev_b32_e32 v130, 2, v12
	v_and_or_b32 v115, v10, s41, v84
	v_addc_co_u32_e32 v45, vcc, 0, v83, vcc
	global_load_dwordx4 v[34:37], v[42:43], off offset:1024 nt
	global_load_dwordx4 v[30:33], v[42:43], off offset:2048 nt
	global_load_dwordx4 v[26:29], v[42:43], off offset:3072 nt
	global_load_dwordx4 v[38:41], v[44:45], off offset:-4096 nt
	global_load_dwordx4 v[22:25], v[44:45], off nt
	global_load_dwordx4 v[18:21], v[44:45], off offset:1024 nt
	global_load_dwordx4 v[14:17], v[44:45], off offset:2048 nt
	global_load_dwordx4 v[10:13], v[44:45], off offset:3072 nt
	s_waitcnt vmcnt(15)
	v_add_f32_e32 v42, v78, v79
	v_add_f32_e32 v43, v80, v81
	v_add_f32_e32 v42, v42, v43
	s_waitcnt vmcnt(14)
	v_add_f32_e32 v43, v74, v75
	v_add_f32_e32 v44, v76, v77
	v_add_f32_e32 v43, v43, v44
	s_waitcnt vmcnt(13)
	v_add_f32_e32 v44, v70, v71
	v_add_f32_e32 v45, v72, v73
	v_add_f32_e32 v44, v44, v45
	s_waitcnt vmcnt(12)
	v_add_f32_e32 v45, v66, v67
	v_add_f32_e32 v49, v68, v69
	v_add_f32_e32 v45, v45, v49
	s_waitcnt vmcnt(11)
	v_add_f32_e32 v49, v62, v63
	v_add_f32_e32 v86, v64, v65
	v_and_b32_e32 v46, 1, v0
	v_add_f32_e32 v49, v49, v86
	s_waitcnt vmcnt(10)
	v_add_f32_e32 v86, v58, v59
	v_add_f32_e32 v88, v60, v61
	v_add_f32_e32 v86, v86, v88
	s_waitcnt vmcnt(9)
	v_add_f32_e32 v88, v54, v55
	v_add_f32_e32 v89, v56, v57
	v_cmp_eq_u32_e64 s[4:5], 1, v46
	v_add_f32_e32 v88, v88, v89
	s_waitcnt vmcnt(8)
	v_add_f32_e32 v89, v50, v51
	v_add_f32_e32 v90, v52, v53
	v_cndmask_b32_e64 v46, v43, v42, s[4:5]
	v_cndmask_b32_e64 v42, v42, v43, s[4:5]
	v_cndmask_b32_e64 v43, v45, v44, s[4:5]
	v_cndmask_b32_e64 v44, v44, v45, s[4:5]
	v_add_f32_e32 v89, v89, v90
	v_cndmask_b32_e64 v45, v49, v86, s[4:5]
	v_add_f32_dpp v43, v43, v44 quad_perm:[1,0,3,2] row_mask:0xf bank_mask:0xf bound_ctrl:1
	v_cndmask_b32_e64 v44, v86, v49, s[4:5]
	v_and_b32_e32 v47, 2, v0
	v_add_f32_dpp v42, v46, v42 quad_perm:[1,0,3,2] row_mask:0xf bank_mask:0xf bound_ctrl:1
	v_add_f32_dpp v44, v44, v45 quad_perm:[1,0,3,2] row_mask:0xf bank_mask:0xf bound_ctrl:1
	v_cndmask_b32_e64 v45, v89, v88, s[4:5]
	v_cndmask_b32_e64 v46, v88, v89, s[4:5]
	v_cmp_eq_u16_e64 s[6:7], 0, v47
	v_and_b32_e32 v48, 4, v0
	v_add_f32_dpp v45, v45, v46 quad_perm:[1,0,3,2] row_mask:0xf bank_mask:0xf bound_ctrl:1
	v_cndmask_b32_e64 v46, v42, v43, s[6:7]
	v_cndmask_b32_e64 v42, v43, v42, s[6:7]
	v_cndmask_b32_e64 v43, v44, v45, s[6:7]
	v_cndmask_b32_e64 v44, v45, v44, s[6:7]
	v_add_f32_dpp v42, v46, v42 quad_perm:[2,3,0,1] row_mask:0xf bank_mask:0xf bound_ctrl:1
	v_cmp_eq_u16_e64 s[8:9], 0, v48
	v_add_f32_dpp v43, v43, v44 quad_perm:[2,3,0,1] row_mask:0xf bank_mask:0xf bound_ctrl:1
	v_lshlrev_b32_e32 v86, 3, v131
	v_cndmask_b32_e64 v44, v42, v43, s[8:9]
	v_cndmask_b32_e64 v42, v43, v42, s[8:9]
	v_mov_b32_e32 v43, v44
	v_and_b32_e32 v87, 8, v87
	v_mov_b32_e32 v116, 0x3727c5ac
	v_mov_b32_dpp v43, v43 row_shl:4 row_mask:0xf bank_mask:0x5
	v_mov_b32_e32 v117, 0x260
	v_bitop3_b32 v141, v125, v0, 4 bitop3:0x36
	v_mov_b32_dpp v43, v44 row_shr:4 row_mask:0xf bank_mask:0xa
	v_add_f32_e32 v42, v42, v43
	v_bitop3_b32 v142, v125, v0, 8 bitop3:0x36
	v_bitop3_b32 v143, v125, v0, 12 bitop3:0x36
	v_add_f32_dpp v42, v42, v42 row_ror:8 row_mask:0xf bank_mask:0xf bound_ctrl:1
	v_mov_b32_e32 v43, v42
	s_nop 1
	v_permlane16_swap_b32_e32 v42, v43
	v_add_f32_e32 v42, v42, v43
	v_mov_b32_e32 v43, v42
	s_nop 1
	v_permlane32_swap_b32_e32 v42, v43
	v_add_f32_e32 v42, v42, v43
	v_mul_f32_e32 v42, 0x3b800000, v42
	s_mov_b32 s3, 0
	v_readlane_b32 s40, v42, 0
	v_readlane_b32 s42, v42, 1
	v_readlane_b32 s44, v42, 2
	v_readlane_b32 s46, v42, 3
	v_readlane_b32 s48, v42, 4
	v_readlane_b32 s50, v42, 5
	v_readlane_b32 s34, v42, 6
	v_readlane_b32 s0, v42, 7
	v_pk_add_f32 v[90:91], v[78:79], s[40:41] op_sel_hi:[1,0] neg_lo:[0,1] neg_hi:[0,1]
	v_pk_add_f32 v[80:81], v[80:81], s[40:41] op_sel_hi:[1,0] neg_lo:[0,1] neg_hi:[0,1]
	v_and_b32_e32 v78, 0x1f0, v86
	v_pk_add_f32 v[76:77], v[76:77], s[42:43] op_sel_hi:[1,0] neg_lo:[0,1] neg_hi:[0,1]
	v_mul_f32_e32 v88, v81, v81
	v_or3_b32 v140, v85, v78, v87
	v_pk_add_f32 v[78:79], v[74:75], s[42:43] op_sel_hi:[1,0] neg_lo:[0,1] neg_hi:[0,1]
	v_mul_f32_e32 v74, v77, v77
	v_fmac_f32_e32 v88, v80, v80
	v_fmac_f32_e32 v74, v76, v76
	v_fmac_f32_e32 v88, v91, v91
	v_fmac_f32_e32 v74, v79, v79
	v_fmac_f32_e32 v88, v90, v90
	v_fmac_f32_e32 v74, v78, v78
	v_cndmask_b32_e64 v75, v74, v88, s[4:5]
	v_cndmask_b32_e64 v74, v88, v74, s[4:5]
	v_mov_b32_e32 v88, 0x1f0
	v_pk_add_f32 v[72:73], v[72:73], s[44:45] op_sel_hi:[1,0] neg_lo:[0,1] neg_hi:[0,1]
	v_add_f32_dpp v89, v75, v74 quad_perm:[1,0,3,2] row_mask:0xf bank_mask:0xf bound_ctrl:1
	v_bitop3_b32 v74, v86, 16, v88 bitop3:0x6c
	v_or3_b32 v138, v85, v74, v87
	v_pk_add_f32 v[74:75], v[70:71], s[44:45] op_sel_hi:[1,0] neg_lo:[0,1] neg_hi:[0,1]
	v_bitop3_b32 v70, v86, 32, v88 bitop3:0x6c
	v_pk_add_f32 v[68:69], v[68:69], s[46:47] op_sel_hi:[1,0] neg_lo:[0,1] neg_hi:[0,1]
	v_mul_f32_e32 v92, v73, v73
	v_or3_b32 v135, v85, v70, v87
	v_pk_add_f32 v[70:71], v[66:67], s[46:47] op_sel_hi:[1,0] neg_lo:[0,1] neg_hi:[0,1]
	v_mul_f32_e32 v66, v69, v69
	v_fmac_f32_e32 v92, v72, v72
	v_fmac_f32_e32 v66, v68, v68
	v_fmac_f32_e32 v92, v75, v75
	v_fmac_f32_e32 v66, v71, v71
	v_fmac_f32_e32 v92, v74, v74
	v_fmac_f32_e32 v66, v70, v70
	v_cndmask_b32_e64 v67, v66, v92, s[4:5]
	v_cndmask_b32_e64 v66, v92, v66, s[4:5]
	v_pk_add_f32 v[64:65], v[64:65], s[48:49] op_sel_hi:[1,0] neg_lo:[0,1] neg_hi:[0,1]
	v_pk_add_f32 v[60:61], v[60:61], s[50:51] op_sel_hi:[1,0] neg_lo:[0,1] neg_hi:[0,1]
	v_add_f32_dpp v66, v67, v66 quad_perm:[1,0,3,2] row_mask:0xf bank_mask:0xf bound_ctrl:1
	v_cndmask_b32_e64 v67, v89, v66, s[6:7]
	v_cndmask_b32_e64 v66, v66, v89, s[6:7]
	v_mul_f32_e32 v92, v65, v65
	v_fmac_f32_e32 v92, v64, v64
	v_add_f32_dpp v89, v67, v66 quad_perm:[2,3,0,1] row_mask:0xf bank_mask:0xf bound_ctrl:1
	v_bitop3_b32 v66, v86, 48, v88 bitop3:0x6c
	v_or3_b32 v134, v85, v66, v87
	v_pk_add_f32 v[66:67], v[62:63], s[48:49] op_sel_hi:[1,0] neg_lo:[0,1] neg_hi:[0,1]
	v_bitop3_b32 v62, v86, 64, v88 bitop3:0x6c
	v_or3_b32 v120, v85, v62, v87
	v_pk_add_f32 v[62:63], v[58:59], s[50:51] op_sel_hi:[1,0] neg_lo:[0,1] neg_hi:[0,1]
	v_mul_f32_e32 v58, v61, v61
	v_fmac_f32_e32 v58, v60, v60
	v_fmac_f32_e32 v92, v67, v67
	v_fmac_f32_e32 v58, v63, v63
	v_fmac_f32_e32 v92, v66, v66
	v_fmac_f32_e32 v58, v62, v62
	v_cndmask_b32_e64 v59, v58, v92, s[4:5]
	v_cndmask_b32_e64 v58, v92, v58, s[4:5]
	v_pk_add_f32 v[56:57], v[56:57], s[34:35] op_sel_hi:[1,0] neg_lo:[0,1] neg_hi:[0,1]
	s_mov_b32 s25, 0x3e6d3387
	v_add_f32_dpp v92, v59, v58 quad_perm:[1,0,3,2] row_mask:0xf bank_mask:0xf bound_ctrl:1
	v_pk_add_f32 v[58:59], v[54:55], s[34:35] op_sel_hi:[1,0] neg_lo:[0,1] neg_hi:[0,1]
	v_pk_add_f32 v[54:55], v[50:51], s[0:1] op_sel_hi:[1,0] neg_lo:[0,1] neg_hi:[0,1]
	v_pk_add_f32 v[50:51], v[52:53], s[0:1] op_sel_hi:[1,0] neg_lo:[0,1] neg_hi:[0,1]
	v_mul_f32_e32 v93, v57, v57
	v_mul_f32_e32 v52, v51, v51
	v_fmac_f32_e32 v93, v56, v56
	v_fmac_f32_e32 v52, v50, v50
	v_fmac_f32_e32 v93, v59, v59
	v_fmac_f32_e32 v52, v55, v55
	v_fmac_f32_e32 v93, v58, v58
	v_fmac_f32_e32 v52, v54, v54
	v_cndmask_b32_e64 v53, v52, v93, s[4:5]
	v_cndmask_b32_e64 v52, v93, v52, s[4:5]
	s_mov_b32 s35, 0xf800000
	s_movk_i32 s0, 0x50
	v_add_f32_dpp v52, v53, v52 quad_perm:[1,0,3,2] row_mask:0xf bank_mask:0xf bound_ctrl:1
	v_cndmask_b32_e64 v53, v92, v52, s[6:7]
	v_cndmask_b32_e64 v52, v52, v92, s[6:7]
	s_mov_b32 s24, 0xbf3a00e3
	s_mov_b32 s22, 0x3f07dc22
	v_add_f32_dpp v52, v53, v52 quad_perm:[2,3,0,1] row_mask:0xf bank_mask:0xf bound_ctrl:1
	v_cndmask_b32_e64 v53, v89, v52, s[8:9]
	v_cndmask_b32_e64 v52, v52, v89, s[8:9]
	v_mov_b32_e32 v89, v53
	s_mov_b32 s34, 0xbe11a98e
	s_mov_b32 s40, 0x3e027906
	v_mov_b32_dpp v89, v89 row_shl:4 row_mask:0xf bank_mask:0x5
	s_mov_b32 s33, 5
	s_nop 0
	v_mov_b32_dpp v89, v53 row_shr:4 row_mask:0xf bank_mask:0xa
	v_add_f32_e32 v52, v52, v89
	v_bitop3_b32 v89, v86, s0, v88 bitop3:0x6c
	v_or3_b32 v121, v85, v89, v87
	v_add_f32_dpp v52, v52, v52 row_ror:8 row_mask:0xf bank_mask:0xf bound_ctrl:1
	v_mov_b32_e32 v53, v52
	s_nop 1
	v_permlane16_swap_b32_e32 v52, v53
	v_add_f32_e32 v52, v52, v53
	v_mov_b32_e32 v53, v52
	s_nop 1
	v_permlane32_swap_b32_e32 v52, v53
	v_add_f32_e32 v52, v52, v53
	v_fmamk_f32 v52, v52, 0x3b800000, v116
	v_mul_f32_e32 v53, 0x4f800000, v52
	v_cmp_gt_f32_e32 vcc, s35, v52
	s_nop 1
	v_cndmask_b32_e32 v52, v52, v53, vcc
	v_sqrt_f32_e32 v53, v52
	s_nop 0
	v_add_u32_e32 v89, -1, v53
	v_fma_f32 v92, -v89, v53, v52
	v_cmp_ge_f32_e64 s[0:1], 0, v92
	v_add_u32_e32 v92, 1, v53
	s_nop 0
	v_cndmask_b32_e64 v89, v53, v89, s[0:1]
	v_fma_f32 v53, -v92, v53, v52
	v_cmp_lt_f32_e64 s[0:1], 0, v53
	s_nop 1
	v_cndmask_b32_e64 v53, v89, v92, s[0:1]
	v_mul_f32_e32 v89, 0x37800000, v53
	v_cndmask_b32_e32 v53, v53, v89, vcc
	v_cmp_class_f32_e32 vcc, v52, v117
	s_nop 1
	v_cndmask_b32_e32 v52, v53, v52, vcc
	v_div_scale_f32 v53, s[0:1], v52, v52, 1.0
	v_rcp_f32_e32 v89, v53
	s_movk_i32 s0, 0x60
	v_bitop3_b32 v92, v86, s0, v88 bitop3:0x6c
	v_or3_b32 v118, v85, v92, v87
	v_fma_f32 v92, -v53, v89, 1.0
	v_fmac_f32_e32 v89, v92, v89
	v_div_scale_f32 v92, vcc, 1.0, v52, 1.0
	v_mul_f32_e32 v93, v92, v89
	v_fma_f32 v94, -v53, v93, v92
	v_fmac_f32_e32 v93, v94, v89
	v_fma_f32 v53, -v53, v93, v92
	v_div_fmas_f32 v53, v53, v89, v93
	v_div_fixup_f32 v52, v53, v52, 1.0
	s_waitcnt vmcnt(4)
	v_add_f32_e32 v89, v38, v39
	v_readlane_b32 s0, v52, 0
	s_nop 1
	v_pk_mul_f32 v[90:91], s[0:1], v[90:91] op_sel_hi:[0,1]
	v_pk_fma_f32 v[92:93], v[90:91], v[238:239], v[242:243]
	v_mov_b64_e32 v[90:91], s[24:25]
	v_fma_f32 v53, |v92|, s25, 1.0
	v_pk_mul_f32 v[98:99], v[92:93], v[92:93]
	v_rcp_f32_e32 v96, v53
	v_mul_f32_e32 v53, 0xbf38aa3b, v98
	v_exp_f32_e32 v98, v53
	v_fma_f32 v53, |v93|, s25, 1.0
	v_rcp_f32_e32 v97, v53
	s_mov_b32 s24, 0x3f35f0e3
	v_pk_mul_f32 v[80:81], s[0:1], v[80:81] op_sel_hi:[0,1]
	v_mul_f32_e32 v53, 0xbf38aa3b, v99
	v_pk_fma_f32 v[100:101], v[96:97], s[22:23], v[90:91] op_sel_hi:[1,0,0]
	v_pk_fma_f32 v[80:81], v[80:81], v[240:241], v[244:245]
	v_pk_fma_f32 v[100:101], v[96:97], v[100:101], s[24:25] op_sel_hi:[1,1,0]
	v_and_b32_e32 v95, 0x7fffffff, v93
	v_pk_fma_f32 v[100:101], v[96:97], v[100:101], s[34:35] op_sel_hi:[1,1,0]
	v_and_b32_e32 v94, 0x7fffffff, v92
	v_pk_fma_f32 v[100:101], v[96:97], v[100:101], s[40:41] op_sel_hi:[1,1,0]
	v_exp_f32_e32 v99, v53
	v_pk_mul_f32 v[96:97], v[96:97], v[100:101]
	v_fma_f32 v53, |v80|, s25, 1.0
	v_pk_mul_f32 v[94:95], v[94:95], v[96:97]
	v_rcp_f32_e32 v96, v53
	v_fma_f32 v53, |v81|, s25, 1.0
	v_rcp_f32_e32 v97, v53
	v_max_f32_e32 v92, 0, v92
	v_max_f32_e32 v93, 0, v93
	v_pk_fma_f32 v[92:93], v[98:99], v[94:95], v[92:93] neg_lo:[1,0,0] neg_hi:[1,0,0]
	v_pk_mul_f32 v[98:99], v[80:81], v[80:81]
	v_pk_fma_f32 v[100:101], v[96:97], s[22:23], v[90:91] op_sel_hi:[1,0,0]
	v_mul_f32_e32 v53, 0xbf38aa3b, v98
	v_exp_f32_e32 v98, v53
	v_pk_fma_f32 v[100:101], v[96:97], v[100:101], s[24:25] op_sel_hi:[1,1,0]
	v_mul_f32_e32 v53, 0xbf38aa3b, v99
	v_pk_fma_f32 v[100:101], v[96:97], v[100:101], s[34:35] op_sel_hi:[1,1,0]
	v_exp_f32_e32 v99, v53
	v_pk_fma_f32 v[100:101], v[96:97], v[100:101], s[40:41] op_sel_hi:[1,1,0]
	v_and_b32_e32 v95, 0x7fffffff, v81
	v_and_b32_e32 v94, 0x7fffffff, v80
	v_pk_mul_f32 v[96:97], v[96:97], v[100:101]
	v_readlane_b32 s0, v52, 1
	v_max_f32_e32 v80, 0, v80
	v_max_f32_e32 v81, 0, v81
	v_pk_mul_f32 v[94:95], v[94:95], v[96:97]
	v_pk_mul_f32 v[78:79], s[0:1], v[78:79] op_sel_hi:[0,1]
	v_pk_fma_f32 v[80:81], v[98:99], v[94:95], v[80:81] neg_lo:[1,0,0] neg_hi:[1,0,0]
	v_pk_fma_f32 v[78:79], v[78:79], v[238:239], v[242:243]
	v_cvt_pk_f16_f32 v92, v92, v93
	v_cvt_pk_f16_f32 v93, v80, v81
	v_fma_f32 v53, |v78|, s25, 1.0
	ds_write_b64 v140, v[92:93] offset:32768
	v_rcp_f32_e32 v92, v53
	v_fma_f32 v53, |v79|, s25, 1.0
	v_rcp_f32_e32 v93, v53
	v_pk_mul_f32 v[94:95], v[78:79], v[78:79]
	v_pk_mul_f32 v[76:77], s[0:1], v[76:77] op_sel_hi:[0,1]
	v_mul_f32_e32 v53, 0xbf38aa3b, v94
	v_pk_fma_f32 v[96:97], v[92:93], s[22:23], v[90:91] op_sel_hi:[1,0,0]
	v_exp_f32_e32 v94, v53
	v_pk_fma_f32 v[96:97], v[92:93], v[96:97], s[24:25] op_sel_hi:[1,1,0]
	v_mul_f32_e32 v53, 0xbf38aa3b, v95
	v_pk_fma_f32 v[96:97], v[92:93], v[96:97], s[34:35] op_sel_hi:[1,1,0]
	v_pk_fma_f32 v[76:77], v[76:77], v[240:241], v[244:245]
	v_pk_fma_f32 v[96:97], v[92:93], v[96:97], s[40:41] op_sel_hi:[1,1,0]
	v_and_b32_e32 v81, 0x7fffffff, v79
	v_and_b32_e32 v80, 0x7fffffff, v78
	v_exp_f32_e32 v95, v53
	v_pk_mul_f32 v[92:93], v[92:93], v[96:97]
	v_fma_f32 v53, |v76|, s25, 1.0
	v_pk_mul_f32 v[80:81], v[80:81], v[92:93]
	v_rcp_f32_e32 v92, v53
	v_fma_f32 v53, |v77|, s25, 1.0
	v_rcp_f32_e32 v93, v53
	v_max_f32_e32 v78, 0, v78
	v_max_f32_e32 v79, 0, v79
	v_pk_fma_f32 v[78:79], v[94:95], v[80:81], v[78:79] neg_lo:[1,0,0] neg_hi:[1,0,0]
	v_pk_mul_f32 v[94:95], v[76:77], v[76:77]
	v_pk_fma_f32 v[96:97], v[92:93], s[22:23], v[90:91] op_sel_hi:[1,0,0]
	v_mul_f32_e32 v53, 0xbf38aa3b, v94
	v_exp_f32_e32 v94, v53
	v_pk_fma_f32 v[96:97], v[92:93], v[96:97], s[24:25] op_sel_hi:[1,1,0]
	v_mul_f32_e32 v53, 0xbf38aa3b, v95
	v_pk_fma_f32 v[96:97], v[92:93], v[96:97], s[34:35] op_sel_hi:[1,1,0]
	v_exp_f32_e32 v95, v53
	v_pk_fma_f32 v[96:97], v[92:93], v[96:97], s[40:41] op_sel_hi:[1,1,0]
	v_and_b32_e32 v81, 0x7fffffff, v77
	v_and_b32_e32 v80, 0x7fffffff, v76
	v_pk_mul_f32 v[92:93], v[92:93], v[96:97]
	v_readlane_b32 s0, v52, 2
	v_max_f32_e32 v76, 0, v76
	v_max_f32_e32 v77, 0, v77
	v_pk_mul_f32 v[80:81], v[80:81], v[92:93]
	v_pk_mul_f32 v[74:75], s[0:1], v[74:75] op_sel_hi:[0,1]
	v_pk_fma_f32 v[76:77], v[94:95], v[80:81], v[76:77] neg_lo:[1,0,0] neg_hi:[1,0,0]
	v_pk_fma_f32 v[74:75], v[74:75], v[238:239], v[242:243]
	v_cvt_pk_f16_f32 v78, v78, v79
	v_cvt_pk_f16_f32 v79, v76, v77
	v_fma_f32 v53, |v74|, s25, 1.0
	ds_write_b64 v138, v[78:79] offset:33280
	v_rcp_f32_e32 v78, v53
	v_fma_f32 v53, |v75|, s25, 1.0
	v_rcp_f32_e32 v79, v53
	v_pk_mul_f32 v[80:81], v[74:75], v[74:75]
	v_pk_mul_f32 v[72:73], s[0:1], v[72:73] op_sel_hi:[0,1]
	v_mul_f32_e32 v53, 0xbf38aa3b, v80
	v_pk_fma_f32 v[92:93], v[78:79], s[22:23], v[90:91] op_sel_hi:[1,0,0]
	v_exp_f32_e32 v80, v53
	v_pk_fma_f32 v[92:93], v[78:79], v[92:93], s[24:25] op_sel_hi:[1,1,0]
	v_mul_f32_e32 v53, 0xbf38aa3b, v81
	v_pk_fma_f32 v[92:93], v[78:79], v[92:93], s[34:35] op_sel_hi:[1,1,0]
	v_pk_fma_f32 v[72:73], v[72:73], v[240:241], v[244:245]
	v_pk_fma_f32 v[92:93], v[78:79], v[92:93], s[40:41] op_sel_hi:[1,1,0]
	v_and_b32_e32 v77, 0x7fffffff, v75
	v_and_b32_e32 v76, 0x7fffffff, v74
	v_exp_f32_e32 v81, v53
	v_pk_mul_f32 v[78:79], v[78:79], v[92:93]
	v_fma_f32 v53, |v72|, s25, 1.0
	v_pk_mul_f32 v[76:77], v[76:77], v[78:79]
	v_rcp_f32_e32 v78, v53
	v_fma_f32 v53, |v73|, s25, 1.0
	v_rcp_f32_e32 v79, v53
	v_max_f32_e32 v74, 0, v74
	v_max_f32_e32 v75, 0, v75
	v_pk_fma_f32 v[74:75], v[80:81], v[76:77], v[74:75] neg_lo:[1,0,0] neg_hi:[1,0,0]
	v_pk_mul_f32 v[80:81], v[72:73], v[72:73]
	v_pk_fma_f32 v[92:93], v[78:79], s[22:23], v[90:91] op_sel_hi:[1,0,0]
	v_mul_f32_e32 v53, 0xbf38aa3b, v80
	v_exp_f32_e32 v80, v53
	v_pk_fma_f32 v[92:93], v[78:79], v[92:93], s[24:25] op_sel_hi:[1,1,0]
	v_mul_f32_e32 v53, 0xbf38aa3b, v81
	v_pk_fma_f32 v[92:93], v[78:79], v[92:93], s[34:35] op_sel_hi:[1,1,0]
	v_exp_f32_e32 v81, v53
	v_pk_fma_f32 v[92:93], v[78:79], v[92:93], s[40:41] op_sel_hi:[1,1,0]
	v_and_b32_e32 v77, 0x7fffffff, v73
	v_and_b32_e32 v76, 0x7fffffff, v72
	v_pk_mul_f32 v[78:79], v[78:79], v[92:93]
	v_readlane_b32 s0, v52, 3
	v_max_f32_e32 v72, 0, v72
	v_max_f32_e32 v73, 0, v73
	v_pk_mul_f32 v[76:77], v[76:77], v[78:79]
	v_pk_mul_f32 v[70:71], s[0:1], v[70:71] op_sel_hi:[0,1]
	v_pk_fma_f32 v[72:73], v[80:81], v[76:77], v[72:73] neg_lo:[1,0,0] neg_hi:[1,0,0]
	v_pk_fma_f32 v[70:71], v[70:71], v[238:239], v[242:243]
	v_cvt_pk_f16_f32 v74, v74, v75
	v_cvt_pk_f16_f32 v75, v72, v73
	v_fma_f32 v53, |v70|, s25, 1.0
	ds_write_b64 v135, v[74:75] offset:33792
	v_rcp_f32_e32 v74, v53
	v_fma_f32 v53, |v71|, s25, 1.0
	v_rcp_f32_e32 v75, v53
	v_pk_mul_f32 v[76:77], v[70:71], v[70:71]
	v_pk_mul_f32 v[68:69], s[0:1], v[68:69] op_sel_hi:[0,1]
	v_mul_f32_e32 v53, 0xbf38aa3b, v76
	v_pk_fma_f32 v[78:79], v[74:75], s[22:23], v[90:91] op_sel_hi:[1,0,0]
	v_exp_f32_e32 v76, v53
	v_pk_fma_f32 v[78:79], v[74:75], v[78:79], s[24:25] op_sel_hi:[1,1,0]
	v_mul_f32_e32 v53, 0xbf38aa3b, v77
	v_pk_fma_f32 v[78:79], v[74:75], v[78:79], s[34:35] op_sel_hi:[1,1,0]
	v_pk_fma_f32 v[68:69], v[68:69], v[240:241], v[244:245]
	v_pk_fma_f32 v[78:79], v[74:75], v[78:79], s[40:41] op_sel_hi:[1,1,0]
	v_and_b32_e32 v73, 0x7fffffff, v71
	v_and_b32_e32 v72, 0x7fffffff, v70
	v_exp_f32_e32 v77, v53
	v_pk_mul_f32 v[74:75], v[74:75], v[78:79]
	v_fma_f32 v53, |v68|, s25, 1.0
	v_pk_mul_f32 v[72:73], v[72:73], v[74:75]
	v_rcp_f32_e32 v74, v53
	v_fma_f32 v53, |v69|, s25, 1.0
	v_rcp_f32_e32 v75, v53
	v_max_f32_e32 v70, 0, v70
	v_max_f32_e32 v71, 0, v71
	v_pk_fma_f32 v[70:71], v[76:77], v[72:73], v[70:71] neg_lo:[1,0,0] neg_hi:[1,0,0]
	v_pk_mul_f32 v[76:77], v[68:69], v[68:69]
	v_pk_fma_f32 v[78:79], v[74:75], s[22:23], v[90:91] op_sel_hi:[1,0,0]
	v_mul_f32_e32 v53, 0xbf38aa3b, v76
	v_exp_f32_e32 v76, v53
	v_pk_fma_f32 v[78:79], v[74:75], v[78:79], s[24:25] op_sel_hi:[1,1,0]
	v_mul_f32_e32 v53, 0xbf38aa3b, v77
	v_pk_fma_f32 v[78:79], v[74:75], v[78:79], s[34:35] op_sel_hi:[1,1,0]
	v_exp_f32_e32 v77, v53
	v_pk_fma_f32 v[78:79], v[74:75], v[78:79], s[40:41] op_sel_hi:[1,1,0]
	v_and_b32_e32 v73, 0x7fffffff, v69
	v_and_b32_e32 v72, 0x7fffffff, v68
	v_pk_mul_f32 v[74:75], v[74:75], v[78:79]
	v_readlane_b32 s0, v52, 4
	v_max_f32_e32 v68, 0, v68
	v_max_f32_e32 v69, 0, v69
	v_pk_mul_f32 v[72:73], v[72:73], v[74:75]
	v_pk_mul_f32 v[66:67], s[0:1], v[66:67] op_sel_hi:[0,1]
	v_pk_fma_f32 v[68:69], v[76:77], v[72:73], v[68:69] neg_lo:[1,0,0] neg_hi:[1,0,0]
	v_pk_fma_f32 v[66:67], v[66:67], v[238:239], v[242:243]
	v_cvt_pk_f16_f32 v70, v70, v71
	v_cvt_pk_f16_f32 v71, v68, v69
	v_fma_f32 v53, |v66|, s25, 1.0
	ds_write_b64 v134, v[70:71] offset:34304
	v_rcp_f32_e32 v70, v53
	v_fma_f32 v53, |v67|, s25, 1.0
	v_rcp_f32_e32 v71, v53
	v_pk_mul_f32 v[72:73], v[66:67], v[66:67]
	v_pk_mul_f32 v[64:65], s[0:1], v[64:65] op_sel_hi:[0,1]
	v_mul_f32_e32 v53, 0xbf38aa3b, v72
	v_pk_fma_f32 v[74:75], v[70:71], s[22:23], v[90:91] op_sel_hi:[1,0,0]
	v_exp_f32_e32 v72, v53
	v_pk_fma_f32 v[74:75], v[70:71], v[74:75], s[24:25] op_sel_hi:[1,1,0]
	v_mul_f32_e32 v53, 0xbf38aa3b, v73
	v_pk_fma_f32 v[74:75], v[70:71], v[74:75], s[34:35] op_sel_hi:[1,1,0]
	v_pk_fma_f32 v[64:65], v[64:65], v[240:241], v[244:245]
	v_pk_fma_f32 v[74:75], v[70:71], v[74:75], s[40:41] op_sel_hi:[1,1,0]
	v_and_b32_e32 v69, 0x7fffffff, v67
	v_and_b32_e32 v68, 0x7fffffff, v66
	v_exp_f32_e32 v73, v53
	v_pk_mul_f32 v[70:71], v[70:71], v[74:75]
	v_fma_f32 v53, |v64|, s25, 1.0
	v_pk_mul_f32 v[68:69], v[68:69], v[70:71]
	v_rcp_f32_e32 v70, v53
	v_fma_f32 v53, |v65|, s25, 1.0
	v_rcp_f32_e32 v71, v53
	v_max_f32_e32 v66, 0, v66
	v_max_f32_e32 v67, 0, v67
	v_pk_fma_f32 v[66:67], v[72:73], v[68:69], v[66:67] neg_lo:[1,0,0] neg_hi:[1,0,0]
	v_pk_mul_f32 v[72:73], v[64:65], v[64:65]
	v_pk_fma_f32 v[74:75], v[70:71], s[22:23], v[90:91] op_sel_hi:[1,0,0]
	v_mul_f32_e32 v53, 0xbf38aa3b, v72
	v_exp_f32_e32 v72, v53
	v_pk_fma_f32 v[74:75], v[70:71], v[74:75], s[24:25] op_sel_hi:[1,1,0]
	v_mul_f32_e32 v53, 0xbf38aa3b, v73
	v_pk_fma_f32 v[74:75], v[70:71], v[74:75], s[34:35] op_sel_hi:[1,1,0]
	v_exp_f32_e32 v73, v53
	v_pk_fma_f32 v[74:75], v[70:71], v[74:75], s[40:41] op_sel_hi:[1,1,0]
	v_and_b32_e32 v69, 0x7fffffff, v65
	v_and_b32_e32 v68, 0x7fffffff, v64
	v_pk_mul_f32 v[70:71], v[70:71], v[74:75]
	v_readlane_b32 s0, v52, 5
	v_max_f32_e32 v64, 0, v64
	v_max_f32_e32 v65, 0, v65
	v_pk_mul_f32 v[68:69], v[68:69], v[70:71]
	v_pk_mul_f32 v[62:63], s[0:1], v[62:63] op_sel_hi:[0,1]
	v_pk_fma_f32 v[64:65], v[72:73], v[68:69], v[64:65] neg_lo:[1,0,0] neg_hi:[1,0,0]
	v_pk_fma_f32 v[62:63], v[62:63], v[238:239], v[242:243]
	v_cvt_pk_f16_f32 v66, v66, v67
	v_cvt_pk_f16_f32 v67, v64, v65
	v_fma_f32 v53, |v62|, s25, 1.0
	ds_write_b64 v120, v[66:67] offset:34816
	v_rcp_f32_e32 v66, v53
	v_fma_f32 v53, |v63|, s25, 1.0
	v_rcp_f32_e32 v67, v53
	v_pk_mul_f32 v[68:69], v[62:63], v[62:63]
	v_pk_mul_f32 v[60:61], s[0:1], v[60:61] op_sel_hi:[0,1]
	v_mul_f32_e32 v53, 0xbf38aa3b, v68
	v_pk_fma_f32 v[70:71], v[66:67], s[22:23], v[90:91] op_sel_hi:[1,0,0]
	v_exp_f32_e32 v68, v53
	v_pk_fma_f32 v[70:71], v[66:67], v[70:71], s[24:25] op_sel_hi:[1,1,0]
	v_mul_f32_e32 v53, 0xbf38aa3b, v69
	v_pk_fma_f32 v[70:71], v[66:67], v[70:71], s[34:35] op_sel_hi:[1,1,0]
	v_pk_fma_f32 v[60:61], v[60:61], v[240:241], v[244:245]
	v_pk_fma_f32 v[70:71], v[66:67], v[70:71], s[40:41] op_sel_hi:[1,1,0]
	v_and_b32_e32 v65, 0x7fffffff, v63
	v_and_b32_e32 v64, 0x7fffffff, v62
	v_exp_f32_e32 v69, v53
	v_pk_mul_f32 v[66:67], v[66:67], v[70:71]
	v_fma_f32 v53, |v60|, s25, 1.0
	v_pk_mul_f32 v[64:65], v[64:65], v[66:67]
	v_rcp_f32_e32 v66, v53
	v_fma_f32 v53, |v61|, s25, 1.0
	v_rcp_f32_e32 v67, v53
	v_max_f32_e32 v62, 0, v62
	v_max_f32_e32 v63, 0, v63
	v_pk_fma_f32 v[62:63], v[68:69], v[64:65], v[62:63] neg_lo:[1,0,0] neg_hi:[1,0,0]
	v_pk_mul_f32 v[68:69], v[60:61], v[60:61]
	v_pk_fma_f32 v[70:71], v[66:67], s[22:23], v[90:91] op_sel_hi:[1,0,0]
	v_mul_f32_e32 v53, 0xbf38aa3b, v68
	v_exp_f32_e32 v68, v53
	v_pk_fma_f32 v[70:71], v[66:67], v[70:71], s[24:25] op_sel_hi:[1,1,0]
	v_mul_f32_e32 v53, 0xbf38aa3b, v69
	v_pk_fma_f32 v[70:71], v[66:67], v[70:71], s[34:35] op_sel_hi:[1,1,0]
	v_exp_f32_e32 v69, v53
	v_pk_fma_f32 v[70:71], v[66:67], v[70:71], s[40:41] op_sel_hi:[1,1,0]
	v_and_b32_e32 v65, 0x7fffffff, v61
	v_and_b32_e32 v64, 0x7fffffff, v60
	v_pk_mul_f32 v[66:67], v[66:67], v[70:71]
	v_readlane_b32 s0, v52, 6
	v_max_f32_e32 v60, 0, v60
	v_max_f32_e32 v61, 0, v61
	v_pk_mul_f32 v[64:65], v[64:65], v[66:67]
	v_pk_mul_f32 v[58:59], s[0:1], v[58:59] op_sel_hi:[0,1]
	v_pk_fma_f32 v[60:61], v[68:69], v[64:65], v[60:61] neg_lo:[1,0,0] neg_hi:[1,0,0]
	v_pk_fma_f32 v[58:59], v[58:59], v[238:239], v[242:243]
	v_cvt_pk_f16_f32 v62, v62, v63
	v_cvt_pk_f16_f32 v63, v60, v61
	v_fma_f32 v53, |v58|, s25, 1.0
	ds_write_b64 v121, v[62:63] offset:35328
	v_rcp_f32_e32 v62, v53
	v_fma_f32 v53, |v59|, s25, 1.0
	v_rcp_f32_e32 v63, v53
	v_pk_mul_f32 v[64:65], v[58:59], v[58:59]
	v_pk_mul_f32 v[56:57], s[0:1], v[56:57] op_sel_hi:[0,1]
	v_mul_f32_e32 v53, 0xbf38aa3b, v64
	v_pk_fma_f32 v[66:67], v[62:63], s[22:23], v[90:91] op_sel_hi:[1,0,0]
	v_exp_f32_e32 v64, v53
	v_pk_fma_f32 v[66:67], v[62:63], v[66:67], s[24:25] op_sel_hi:[1,1,0]
	v_mul_f32_e32 v53, 0xbf38aa3b, v65
	v_pk_fma_f32 v[66:67], v[62:63], v[66:67], s[34:35] op_sel_hi:[1,1,0]
	v_pk_fma_f32 v[56:57], v[56:57], v[240:241], v[244:245]
	v_pk_fma_f32 v[66:67], v[62:63], v[66:67], s[40:41] op_sel_hi:[1,1,0]
	v_and_b32_e32 v61, 0x7fffffff, v59
	v_and_b32_e32 v60, 0x7fffffff, v58
	v_exp_f32_e32 v65, v53
	v_pk_mul_f32 v[62:63], v[62:63], v[66:67]
	v_fma_f32 v53, |v56|, s25, 1.0
	v_pk_mul_f32 v[60:61], v[60:61], v[62:63]
	v_rcp_f32_e32 v62, v53
	v_fma_f32 v53, |v57|, s25, 1.0
	v_rcp_f32_e32 v63, v53
	v_max_f32_e32 v58, 0, v58
	v_max_f32_e32 v59, 0, v59
	v_pk_fma_f32 v[58:59], v[64:65], v[60:61], v[58:59] neg_lo:[1,0,0] neg_hi:[1,0,0]
	v_pk_mul_f32 v[64:65], v[56:57], v[56:57]
	v_pk_fma_f32 v[66:67], v[62:63], s[22:23], v[90:91] op_sel_hi:[1,0,0]
	v_mul_f32_e32 v53, 0xbf38aa3b, v64
	v_exp_f32_e32 v64, v53
	v_pk_fma_f32 v[66:67], v[62:63], v[66:67], s[24:25] op_sel_hi:[1,1,0]
	v_mul_f32_e32 v53, 0xbf38aa3b, v65
	v_pk_fma_f32 v[66:67], v[62:63], v[66:67], s[34:35] op_sel_hi:[1,1,0]
	v_exp_f32_e32 v65, v53
	v_pk_fma_f32 v[66:67], v[62:63], v[66:67], s[40:41] op_sel_hi:[1,1,0]
	v_and_b32_e32 v61, 0x7fffffff, v57
	v_and_b32_e32 v60, 0x7fffffff, v56
	v_pk_mul_f32 v[62:63], v[62:63], v[66:67]
	v_readlane_b32 s0, v52, 7
	v_max_f32_e32 v56, 0, v56
	v_max_f32_e32 v57, 0, v57
	v_pk_mul_f32 v[60:61], v[60:61], v[62:63]
	v_pk_mul_f32 v[52:53], s[0:1], v[54:55] op_sel_hi:[0,1]
	v_pk_fma_f32 v[56:57], v[64:65], v[60:61], v[56:57] neg_lo:[1,0,0] neg_hi:[1,0,0]
	v_pk_fma_f32 v[52:53], v[52:53], v[238:239], v[242:243]
	v_cvt_pk_f16_f32 v58, v58, v59
	v_cvt_pk_f16_f32 v59, v56, v57
	v_fma_f32 v56, |v52|, s25, 1.0
	v_fma_f32 v57, |v53|, s25, 1.0
	v_rcp_f32_e32 v56, v56
	v_rcp_f32_e32 v57, v57
	ds_write_b64 v118, v[58:59] offset:35840
	v_pk_mul_f32 v[58:59], v[52:53], v[52:53]
	v_and_b32_e32 v55, 0x7fffffff, v53
	v_pk_fma_f32 v[60:61], v[56:57], s[22:23], v[90:91] op_sel_hi:[1,0,0]
	v_mul_f32_e32 v58, 0xbf38aa3b, v58
	v_pk_fma_f32 v[60:61], v[56:57], v[60:61], s[24:25] op_sel_hi:[1,1,0]
	v_mul_f32_e32 v59, 0xbf38aa3b, v59
	v_exp_f32_e32 v58, v58
	v_pk_fma_f32 v[60:61], v[56:57], v[60:61], s[34:35] op_sel_hi:[1,1,0]
	v_exp_f32_e32 v59, v59
	v_pk_fma_f32 v[60:61], v[56:57], v[60:61], s[40:41] op_sel_hi:[1,1,0]
	v_and_b32_e32 v54, 0x7fffffff, v52
	v_pk_mul_f32 v[56:57], v[56:57], v[60:61]
	v_max_f32_e32 v52, 0, v52
	v_max_f32_e32 v53, 0, v53
	v_pk_mul_f32 v[54:55], v[54:55], v[56:57]
	v_pk_mul_f32 v[50:51], s[0:1], v[50:51] op_sel_hi:[0,1]
	v_pk_fma_f32 v[52:53], v[58:59], v[54:55], v[52:53] neg_lo:[1,0,0] neg_hi:[1,0,0]
	v_pk_fma_f32 v[50:51], v[50:51], v[240:241], v[244:245]
	v_cvt_pk_f16_f32 v52, v52, v53
	v_fma_f32 v53, |v50|, s25, 1.0
	v_rcp_f32_e32 v56, v53
	v_fma_f32 v53, |v51|, s25, 1.0
	v_rcp_f32_e32 v57, v53
	v_pk_mul_f32 v[58:59], v[50:51], v[50:51]
	v_and_b32_e32 v55, 0x7fffffff, v51
	v_mul_f32_e32 v53, 0xbf38aa3b, v58
	v_pk_fma_f32 v[60:61], v[56:57], s[22:23], v[90:91] op_sel_hi:[1,0,0]
	v_exp_f32_e32 v58, v53
	v_pk_fma_f32 v[60:61], v[56:57], v[60:61], s[24:25] op_sel_hi:[1,1,0]
	v_mul_f32_e32 v53, 0xbf38aa3b, v59
	v_pk_fma_f32 v[60:61], v[56:57], v[60:61], s[34:35] op_sel_hi:[1,1,0]
	v_exp_f32_e32 v59, v53
	v_pk_fma_f32 v[60:61], v[56:57], v[60:61], s[40:41] op_sel_hi:[1,1,0]
	v_and_b32_e32 v54, 0x7fffffff, v50
	v_pk_mul_f32 v[56:57], v[56:57], v[60:61]
	v_max_f32_e32 v50, 0, v50
	v_max_f32_e32 v51, 0, v51
	v_pk_mul_f32 v[54:55], v[54:55], v[56:57]
	s_movk_i32 s0, 0x70
	v_pk_fma_f32 v[50:51], v[58:59], v[54:55], v[50:51] neg_lo:[1,0,0] neg_hi:[1,0,0]
	s_waitcnt vmcnt(0)
	v_add_f32_e32 v96, v24, v25
	v_cvt_pk_f16_f32 v53, v50, v51
	v_bitop3_b32 v50, v86, s0, v88 bitop3:0x6c
	s_movk_i32 s0, 0x4000
	v_add_co_u32_e32 v92, vcc, s0, v82
	s_movk_i32 s0, 0x5000
	s_nop 0
	v_addc_co_u32_e32 v93, vcc, 0, v83, vcc
	v_or3_b32 v144, v85, v50, v87
	v_add_co_u32_e32 v94, vcc, s0, v82
	ds_write_b64 v144, v[52:53] offset:36352
	s_nop 0
	v_addc_co_u32_e32 v95, vcc, 0, v83, vcc
	s_movk_i32 s56, 0x5000
	v_add_co_u32_e64 v234, s[58:59], s56, v82
	s_nop 1
	v_addc_co_u32_e64 v235, s[58:59], 0, v83, s[58:59]
	global_load_dwordx4 v[170:173], v[234:235], off offset:-4096 nt
	global_load_dwordx4 v[174:177], v[234:235], off offset:-3072 nt
	global_load_dwordx4 v[178:181], v[234:235], off offset:-2048 nt
	global_load_dwordx4 v[182:185], v[234:235], off offset:-1024 nt
	global_load_dwordx4 v[186:189], v[234:235], off nt
	global_load_dwordx4 v[190:193], v[234:235], off offset:1024 nt
	global_load_dwordx4 v[194:197], v[234:235], off offset:2048 nt
	global_load_dwordx4 v[198:201], v[234:235], off offset:3072 nt
	v_add_f32_e32 v92, v40, v41
	v_add_f32_e32 v89, v89, v92
	v_add_f32_e32 v92, v34, v35
	v_add_f32_e32 v93, v36, v37
	v_add_f32_e32 v92, v92, v93
	v_add_f32_e32 v93, v30, v31
	v_add_f32_e32 v94, v32, v33
	v_add_f32_e32 v93, v93, v94
	v_add_f32_e32 v94, v26, v27
	v_add_f32_e32 v95, v28, v29
	v_add_f32_e32 v94, v94, v95
	v_add_f32_e32 v95, v22, v23
	v_add_f32_e32 v95, v95, v96
	v_add_f32_e32 v96, v18, v19
	v_add_f32_e32 v97, v20, v21
	v_add_f32_e32 v96, v96, v97
	v_add_f32_e32 v97, v14, v15
	v_add_f32_e32 v98, v16, v17
	v_add_f32_e32 v97, v97, v98
	v_add_f32_e32 v98, v10, v11
	v_add_f32_e32 v99, v12, v13
	v_add_f32_e32 v98, v98, v99
	v_cndmask_b32_e64 v99, v92, v89, s[4:5]
	v_cndmask_b32_e64 v89, v89, v92, s[4:5]
	v_cndmask_b32_e64 v92, v94, v93, s[4:5]
	v_cndmask_b32_e64 v93, v93, v94, s[4:5]
	v_cndmask_b32_e64 v94, v95, v96, s[4:5]
	v_add_f32_dpp v89, v99, v89 quad_perm:[1,0,3,2] row_mask:0xf bank_mask:0xf bound_ctrl:1
	v_add_f32_dpp v92, v92, v93 quad_perm:[1,0,3,2] row_mask:0xf bank_mask:0xf bound_ctrl:1
	v_cndmask_b32_e64 v93, v96, v95, s[4:5]
	v_cndmask_b32_e64 v95, v97, v98, s[4:5]
	s_movk_i32 s1, 0x80
	v_add_f32_dpp v93, v93, v94 quad_perm:[1,0,3,2] row_mask:0xf bank_mask:0xf bound_ctrl:1
	v_cndmask_b32_e64 v94, v98, v97, s[4:5]
	s_movk_i32 s23, 0x90
	s_nop 0
	v_add_f32_dpp v94, v94, v95 quad_perm:[1,0,3,2] row_mask:0xf bank_mask:0xf bound_ctrl:1
	v_cndmask_b32_e64 v95, v89, v92, s[6:7]
	v_cndmask_b32_e64 v89, v92, v89, s[6:7]
	v_cndmask_b32_e64 v92, v93, v94, s[6:7]
	v_cndmask_b32_e64 v93, v94, v93, s[6:7]
	v_add_f32_dpp v89, v95, v89 quad_perm:[2,3,0,1] row_mask:0xf bank_mask:0xf bound_ctrl:1
	s_nop 0
	v_add_f32_dpp v92, v92, v93 quad_perm:[2,3,0,1] row_mask:0xf bank_mask:0xf bound_ctrl:1
	v_cndmask_b32_e64 v93, v89, v92, s[8:9]
	v_cndmask_b32_e64 v89, v92, v89, s[8:9]
	v_mov_b32_e32 v92, v93
	s_nop 1
	v_mov_b32_dpp v92, v92 row_shl:4 row_mask:0xf bank_mask:0x5
	s_nop 1
	v_mov_b32_dpp v92, v93 row_shr:4 row_mask:0xf bank_mask:0xa
	v_add_f32_e32 v89, v89, v92
	s_nop 1
	v_add_f32_dpp v89, v89, v89 row_ror:8 row_mask:0xf bank_mask:0xf bound_ctrl:1
	v_mov_b32_e32 v92, v89
	s_nop 1
	v_permlane16_swap_b32_e32 v89, v92
	v_add_f32_e32 v89, v89, v92
	v_mov_b32_e32 v92, v89
	s_nop 1
	v_permlane32_swap_b32_e32 v89, v92
	v_add_f32_e32 v89, v89, v92
	v_mul_f32_e32 v89, 0x3b800000, v89
	v_bitop3_b32 v92, v86, s1, v88 bitop3:0x6c
	v_readlane_b32 s44, v89, 0
	v_readlane_b32 s46, v89, 1
	v_readlane_b32 s48, v89, 2
	v_pk_add_f32 v[40:41], v[40:41], s[44:45] op_sel_hi:[1,0] neg_lo:[0,1] neg_hi:[0,1]
	v_pk_add_f32 v[36:37], v[36:37], s[46:47] op_sel_hi:[1,0] neg_lo:[0,1] neg_hi:[0,1]
	v_readlane_b32 s50, v89, 3
	v_readlane_b32 s52, v89, 4
	v_readlane_b32 s54, v89, 5
	v_readlane_b32 s42, v89, 6
	v_readlane_b32 s0, v89, 7
	v_mul_f32_e32 v89, v41, v41
	v_or3_b32 v145, v85, v92, v87
	v_pk_add_f32 v[92:93], v[34:35], s[46:47] op_sel_hi:[1,0] neg_lo:[0,1] neg_hi:[0,1]
	v_mul_f32_e32 v34, v37, v37
	v_pk_add_f32 v[38:39], v[38:39], s[44:45] op_sel_hi:[1,0] neg_lo:[0,1] neg_hi:[0,1]
	v_fmac_f32_e32 v89, v40, v40
	v_fmac_f32_e32 v34, v36, v36
	v_fmac_f32_e32 v89, v39, v39
	v_fmac_f32_e32 v34, v93, v93
	v_fmac_f32_e32 v89, v38, v38
	v_fmac_f32_e32 v34, v92, v92
	v_cndmask_b32_e64 v35, v34, v89, s[4:5]
	v_cndmask_b32_e64 v34, v89, v34, s[4:5]
	s_movk_i32 s1, 0xa0
	v_pk_add_f32 v[32:33], v[32:33], s[48:49] op_sel_hi:[1,0] neg_lo:[0,1] neg_hi:[0,1]
	v_add_f32_dpp v89, v35, v34 quad_perm:[1,0,3,2] row_mask:0xf bank_mask:0xf bound_ctrl:1
	v_bitop3_b32 v34, v86, s23, v88 bitop3:0x6c
	v_or3_b32 v139, v85, v34, v87
	v_pk_add_f32 v[34:35], v[30:31], s[48:49] op_sel_hi:[1,0] neg_lo:[0,1] neg_hi:[0,1]
	v_bitop3_b32 v30, v86, s1, v88 bitop3:0x6c
	v_pk_add_f32 v[28:29], v[28:29], s[50:51] op_sel_hi:[1,0] neg_lo:[0,1] neg_hi:[0,1]
	v_mul_f32_e32 v94, v33, v33
	v_or3_b32 v137, v85, v30, v87
	v_pk_add_f32 v[30:31], v[26:27], s[50:51] op_sel_hi:[1,0] neg_lo:[0,1] neg_hi:[0,1]
	v_mul_f32_e32 v26, v29, v29
	v_fmac_f32_e32 v94, v32, v32
	v_fmac_f32_e32 v26, v28, v28
	v_fmac_f32_e32 v94, v35, v35
	v_fmac_f32_e32 v26, v31, v31
	v_fmac_f32_e32 v94, v34, v34
	v_fmac_f32_e32 v26, v30, v30
	v_cndmask_b32_e64 v27, v26, v94, s[4:5]
	v_cndmask_b32_e64 v26, v94, v26, s[4:5]
	s_movk_i32 s1, 0xb0
	v_pk_add_f32 v[24:25], v[24:25], s[52:53] op_sel_hi:[1,0] neg_lo:[0,1] neg_hi:[0,1]
	v_add_f32_dpp v26, v27, v26 quad_perm:[1,0,3,2] row_mask:0xf bank_mask:0xf bound_ctrl:1
	v_cndmask_b32_e64 v27, v89, v26, s[6:7]
	v_cndmask_b32_e64 v26, v26, v89, s[6:7]
	v_pk_add_f32 v[20:21], v[20:21], s[54:55] op_sel_hi:[1,0] neg_lo:[0,1] neg_hi:[0,1]
	v_mul_f32_e32 v94, v25, v25
	v_add_f32_dpp v89, v27, v26 quad_perm:[2,3,0,1] row_mask:0xf bank_mask:0xf bound_ctrl:1
	v_bitop3_b32 v26, v86, s1, v88 bitop3:0x6c
	s_movk_i32 s1, 0xc0
	v_or3_b32 v136, v85, v26, v87
	v_pk_add_f32 v[26:27], v[22:23], s[52:53] op_sel_hi:[1,0] neg_lo:[0,1] neg_hi:[0,1]
	v_bitop3_b32 v22, v86, s1, v88 bitop3:0x6c
	v_or3_b32 v123, v85, v22, v87
	v_pk_add_f32 v[22:23], v[18:19], s[54:55] op_sel_hi:[1,0] neg_lo:[0,1] neg_hi:[0,1]
	v_mul_f32_e32 v18, v21, v21
	v_fmac_f32_e32 v94, v24, v24
	v_fmac_f32_e32 v18, v20, v20
	v_fmac_f32_e32 v94, v27, v27
	v_fmac_f32_e32 v18, v23, v23
	v_fmac_f32_e32 v94, v26, v26
	v_fmac_f32_e32 v18, v22, v22
	v_cndmask_b32_e64 v19, v18, v94, s[4:5]
	v_cndmask_b32_e64 v18, v94, v18, s[4:5]
	v_pk_add_f32 v[16:17], v[16:17], s[42:43] op_sel_hi:[1,0] neg_lo:[0,1] neg_hi:[0,1]
	s_nop 0
	v_add_f32_dpp v94, v19, v18 quad_perm:[1,0,3,2] row_mask:0xf bank_mask:0xf bound_ctrl:1
	v_pk_add_f32 v[18:19], v[14:15], s[42:43] op_sel_hi:[1,0] neg_lo:[0,1] neg_hi:[0,1]
	v_pk_add_f32 v[14:15], v[10:11], s[0:1] op_sel_hi:[1,0] neg_lo:[0,1] neg_hi:[0,1]
	v_pk_add_f32 v[10:11], v[12:13], s[0:1] op_sel_hi:[1,0] neg_lo:[0,1] neg_hi:[0,1]
	v_mul_f32_e32 v95, v17, v17
	v_mul_f32_e32 v12, v11, v11
	v_fmac_f32_e32 v95, v16, v16
	v_fmac_f32_e32 v12, v10, v10
	v_fmac_f32_e32 v95, v19, v19
	v_fmac_f32_e32 v12, v15, v15
	v_fmac_f32_e32 v95, v18, v18
	v_fmac_f32_e32 v12, v14, v14
	v_cndmask_b32_e64 v13, v12, v95, s[4:5]
	v_cndmask_b32_e64 v12, v95, v12, s[4:5]
	s_movk_i32 s0, 0xd0
	s_nop 0
	v_add_f32_dpp v12, v13, v12 quad_perm:[1,0,3,2] row_mask:0xf bank_mask:0xf bound_ctrl:1
	v_cndmask_b32_e64 v13, v94, v12, s[6:7]
	v_cndmask_b32_e64 v12, v12, v94, s[6:7]
	s_nop 1
	v_add_f32_dpp v12, v13, v12 quad_perm:[2,3,0,1] row_mask:0xf bank_mask:0xf bound_ctrl:1
	v_cndmask_b32_e64 v13, v89, v12, s[8:9]
	v_cndmask_b32_e64 v12, v12, v89, s[8:9]
	v_mov_b32_e32 v89, v13
	s_nop 1
	v_mov_b32_dpp v89, v89 row_shl:4 row_mask:0xf bank_mask:0x5
	s_nop 1
	v_mov_b32_dpp v89, v13 row_shr:4 row_mask:0xf bank_mask:0xa
	v_add_f32_e32 v12, v12, v89
	v_bitop3_b32 v89, v86, s0, v88 bitop3:0x6c
	v_or3_b32 v133, v85, v89, v87
	v_add_f32_dpp v12, v12, v12 row_ror:8 row_mask:0xf bank_mask:0xf bound_ctrl:1
	v_mov_b32_e32 v13, v12
	s_nop 1
	v_permlane16_swap_b32_e32 v12, v13
	v_add_f32_e32 v12, v12, v13
	v_mov_b32_e32 v13, v12
	s_nop 1
	v_permlane32_swap_b32_e32 v12, v13
	v_add_f32_e32 v12, v12, v13
	v_fmamk_f32 v12, v12, 0x3b800000, v116
	v_mul_f32_e32 v13, 0x4f800000, v12
	v_cmp_gt_f32_e32 vcc, s35, v12
	s_nop 1
	v_cndmask_b32_e32 v12, v12, v13, vcc
	v_sqrt_f32_e32 v13, v12
	s_nop 0
	v_add_u32_e32 v89, -1, v13
	v_fma_f32 v94, -v89, v13, v12
	v_cmp_ge_f32_e64 s[0:1], 0, v94
	v_add_u32_e32 v94, 1, v13
	s_nop 0
	v_cndmask_b32_e64 v89, v13, v89, s[0:1]
	v_fma_f32 v13, -v94, v13, v12
	v_cmp_lt_f32_e64 s[0:1], 0, v13
	s_nop 1
	v_cndmask_b32_e64 v13, v89, v94, s[0:1]
	v_mul_f32_e32 v89, 0x37800000, v13
	v_cndmask_b32_e32 v13, v13, v89, vcc
	v_cmp_class_f32_e32 vcc, v12, v117
	s_nop 1
	v_cndmask_b32_e32 v12, v13, v12, vcc
	v_div_scale_f32 v13, s[0:1], v12, v12, 1.0
	v_rcp_f32_e32 v89, v13
	s_movk_i32 s0, 0xe0
	v_bitop3_b32 v94, v86, s0, v88 bitop3:0x6c
	v_or3_b32 v119, v85, v94, v87
	v_fma_f32 v94, -v13, v89, 1.0
	v_fmac_f32_e32 v89, v94, v89
	v_div_scale_f32 v94, vcc, 1.0, v12, 1.0
	v_mul_f32_e32 v95, v94, v89
	v_fma_f32 v96, -v13, v95, v94
	v_fmac_f32_e32 v95, v96, v89
	v_fma_f32 v13, -v13, v95, v94
	v_div_fmas_f32 v13, v13, v89, v95
	v_div_fixup_f32 v12, v13, v12, 1.0
	s_nop 0
	v_readlane_b32 s0, v12, 0
	s_nop 1
	v_pk_mul_f32 v[38:39], s[0:1], v[38:39] op_sel_hi:[0,1]
	v_pk_fma_f32 v[38:39], v[38:39], v[238:239], v[242:243]
	v_pk_mul_f32 v[40:41], s[0:1], v[40:41] op_sel_hi:[0,1]
	v_fma_f32 v13, |v38|, s25, 1.0
	v_rcp_f32_e32 v96, v13
	v_fma_f32 v13, |v39|, s25, 1.0
	v_rcp_f32_e32 v97, v13
	v_pk_mul_f32 v[98:99], v[38:39], v[38:39]
	v_pk_fma_f32 v[40:41], v[40:41], v[240:241], v[244:245]
	v_mul_f32_e32 v13, 0xbf38aa3b, v98
	v_pk_fma_f32 v[100:101], v[96:97], s[22:23], v[90:91] op_sel_hi:[1,0,0]
	v_exp_f32_e32 v98, v13
	v_pk_fma_f32 v[100:101], v[96:97], v[100:101], s[24:25] op_sel_hi:[1,1,0]
	v_mul_f32_e32 v13, 0xbf38aa3b, v99
	v_pk_fma_f32 v[100:101], v[96:97], v[100:101], s[34:35] op_sel_hi:[1,1,0]
	v_and_b32_e32 v95, 0x7fffffff, v39
	v_pk_fma_f32 v[100:101], v[96:97], v[100:101], s[40:41] op_sel_hi:[1,1,0]
	v_and_b32_e32 v94, 0x7fffffff, v38
	v_exp_f32_e32 v99, v13
	v_pk_mul_f32 v[96:97], v[96:97], v[100:101]
	v_fma_f32 v13, |v40|, s25, 1.0
	v_pk_mul_f32 v[94:95], v[94:95], v[96:97]
	v_rcp_f32_e32 v96, v13
	v_fma_f32 v13, |v41|, s25, 1.0
	v_rcp_f32_e32 v97, v13
	v_max_f32_e32 v38, 0, v38
	v_max_f32_e32 v39, 0, v39
	v_pk_fma_f32 v[38:39], v[98:99], v[94:95], v[38:39] neg_lo:[1,0,0] neg_hi:[1,0,0]
	v_pk_mul_f32 v[98:99], v[40:41], v[40:41]
	v_pk_fma_f32 v[100:101], v[96:97], s[22:23], v[90:91] op_sel_hi:[1,0,0]
	v_mul_f32_e32 v13, 0xbf38aa3b, v98
	v_exp_f32_e32 v98, v13
	v_pk_fma_f32 v[100:101], v[96:97], v[100:101], s[24:25] op_sel_hi:[1,1,0]
	v_mul_f32_e32 v13, 0xbf38aa3b, v99
	v_pk_fma_f32 v[100:101], v[96:97], v[100:101], s[34:35] op_sel_hi:[1,1,0]
	v_exp_f32_e32 v99, v13
	v_pk_fma_f32 v[100:101], v[96:97], v[100:101], s[40:41] op_sel_hi:[1,1,0]
	v_and_b32_e32 v95, 0x7fffffff, v41
	v_and_b32_e32 v94, 0x7fffffff, v40
	v_pk_mul_f32 v[96:97], v[96:97], v[100:101]
	v_max_f32_e32 v40, 0, v40
	v_max_f32_e32 v41, 0, v41
	v_pk_mul_f32 v[94:95], v[94:95], v[96:97]
	v_cvt_pk_f16_f32 v38, v38, v39
	v_pk_fma_f32 v[40:41], v[98:99], v[94:95], v[40:41] neg_lo:[1,0,0] neg_hi:[1,0,0]
	v_readlane_b32 s0, v12, 1
	v_cvt_pk_f16_f32 v39, v40, v41
	ds_write_b64 v145, v[38:39] offset:36864
	v_pk_mul_f32 v[38:39], s[0:1], v[92:93] op_sel_hi:[0,1]
	v_pk_fma_f32 v[38:39], v[38:39], v[238:239], v[242:243]
	v_pk_mul_f32 v[36:37], s[0:1], v[36:37] op_sel_hi:[0,1]
	v_fma_f32 v13, |v38|, s25, 1.0
	v_rcp_f32_e32 v92, v13
	v_fma_f32 v13, |v39|, s25, 1.0
	v_rcp_f32_e32 v93, v13
	v_pk_mul_f32 v[94:95], v[38:39], v[38:39]
	v_pk_fma_f32 v[36:37], v[36:37], v[240:241], v[244:245]
	v_mul_f32_e32 v13, 0xbf38aa3b, v94
	v_pk_fma_f32 v[96:97], v[92:93], s[22:23], v[90:91] op_sel_hi:[1,0,0]
	v_exp_f32_e32 v94, v13
	v_pk_fma_f32 v[96:97], v[92:93], v[96:97], s[24:25] op_sel_hi:[1,1,0]
	v_mul_f32_e32 v13, 0xbf38aa3b, v95
	v_pk_fma_f32 v[96:97], v[92:93], v[96:97], s[34:35] op_sel_hi:[1,1,0]
	v_and_b32_e32 v41, 0x7fffffff, v39
	v_pk_fma_f32 v[96:97], v[92:93], v[96:97], s[40:41] op_sel_hi:[1,1,0]
	v_and_b32_e32 v40, 0x7fffffff, v38
	v_exp_f32_e32 v95, v13
	v_pk_mul_f32 v[92:93], v[92:93], v[96:97]
	v_fma_f32 v13, |v36|, s25, 1.0
	v_pk_mul_f32 v[40:41], v[40:41], v[92:93]
	v_rcp_f32_e32 v92, v13
	v_fma_f32 v13, |v37|, s25, 1.0
	v_rcp_f32_e32 v93, v13
	v_max_f32_e32 v38, 0, v38
	v_max_f32_e32 v39, 0, v39
	v_pk_fma_f32 v[38:39], v[94:95], v[40:41], v[38:39] neg_lo:[1,0,0] neg_hi:[1,0,0]
	v_pk_mul_f32 v[94:95], v[36:37], v[36:37]
	v_pk_fma_f32 v[96:97], v[92:93], s[22:23], v[90:91] op_sel_hi:[1,0,0]
	v_mul_f32_e32 v13, 0xbf38aa3b, v94
	v_exp_f32_e32 v94, v13
	v_pk_fma_f32 v[96:97], v[92:93], v[96:97], s[24:25] op_sel_hi:[1,1,0]
	v_mul_f32_e32 v13, 0xbf38aa3b, v95
	v_pk_fma_f32 v[96:97], v[92:93], v[96:97], s[34:35] op_sel_hi:[1,1,0]
	v_exp_f32_e32 v95, v13
	v_pk_fma_f32 v[96:97], v[92:93], v[96:97], s[40:41] op_sel_hi:[1,1,0]
	v_and_b32_e32 v41, 0x7fffffff, v37
	v_and_b32_e32 v40, 0x7fffffff, v36
	v_pk_mul_f32 v[92:93], v[92:93], v[96:97]
	v_readlane_b32 s0, v12, 2
	v_max_f32_e32 v36, 0, v36
	v_max_f32_e32 v37, 0, v37
	v_pk_mul_f32 v[40:41], v[40:41], v[92:93]
	v_pk_mul_f32 v[34:35], s[0:1], v[34:35] op_sel_hi:[0,1]
	v_pk_fma_f32 v[36:37], v[94:95], v[40:41], v[36:37] neg_lo:[1,0,0] neg_hi:[1,0,0]
	v_pk_fma_f32 v[34:35], v[34:35], v[238:239], v[242:243]
	v_cvt_pk_f16_f32 v38, v38, v39
	v_cvt_pk_f16_f32 v39, v36, v37
	v_fma_f32 v13, |v34|, s25, 1.0
	ds_write_b64 v139, v[38:39] offset:37376
	v_rcp_f32_e32 v38, v13
	v_fma_f32 v13, |v35|, s25, 1.0
	v_rcp_f32_e32 v39, v13
	v_pk_mul_f32 v[40:41], v[34:35], v[34:35]
	v_pk_mul_f32 v[32:33], s[0:1], v[32:33] op_sel_hi:[0,1]
	v_mul_f32_e32 v13, 0xbf38aa3b, v40
	v_pk_fma_f32 v[92:93], v[38:39], s[22:23], v[90:91] op_sel_hi:[1,0,0]
	v_exp_f32_e32 v40, v13
	v_pk_fma_f32 v[92:93], v[38:39], v[92:93], s[24:25] op_sel_hi:[1,1,0]
	v_mul_f32_e32 v13, 0xbf38aa3b, v41
	v_pk_fma_f32 v[92:93], v[38:39], v[92:93], s[34:35] op_sel_hi:[1,1,0]
	v_pk_fma_f32 v[32:33], v[32:33], v[240:241], v[244:245]
	v_pk_fma_f32 v[92:93], v[38:39], v[92:93], s[40:41] op_sel_hi:[1,1,0]
	v_and_b32_e32 v37, 0x7fffffff, v35
	v_and_b32_e32 v36, 0x7fffffff, v34
	v_exp_f32_e32 v41, v13
	v_pk_mul_f32 v[38:39], v[38:39], v[92:93]
	v_fma_f32 v13, |v32|, s25, 1.0
	v_pk_mul_f32 v[36:37], v[36:37], v[38:39]
	v_rcp_f32_e32 v38, v13
	v_fma_f32 v13, |v33|, s25, 1.0
	v_rcp_f32_e32 v39, v13
	v_max_f32_e32 v34, 0, v34
	v_max_f32_e32 v35, 0, v35
	v_pk_fma_f32 v[34:35], v[40:41], v[36:37], v[34:35] neg_lo:[1,0,0] neg_hi:[1,0,0]
	v_pk_mul_f32 v[40:41], v[32:33], v[32:33]
	v_pk_fma_f32 v[92:93], v[38:39], s[22:23], v[90:91] op_sel_hi:[1,0,0]
	v_mul_f32_e32 v13, 0xbf38aa3b, v40
	v_exp_f32_e32 v40, v13
	v_pk_fma_f32 v[92:93], v[38:39], v[92:93], s[24:25] op_sel_hi:[1,1,0]
	v_mul_f32_e32 v13, 0xbf38aa3b, v41
	v_pk_fma_f32 v[92:93], v[38:39], v[92:93], s[34:35] op_sel_hi:[1,1,0]
	v_exp_f32_e32 v41, v13
	v_pk_fma_f32 v[92:93], v[38:39], v[92:93], s[40:41] op_sel_hi:[1,1,0]
	v_and_b32_e32 v37, 0x7fffffff, v33
	v_and_b32_e32 v36, 0x7fffffff, v32
	v_pk_mul_f32 v[38:39], v[38:39], v[92:93]
	v_readlane_b32 s0, v12, 3
	v_max_f32_e32 v32, 0, v32
	v_max_f32_e32 v33, 0, v33
	v_pk_mul_f32 v[36:37], v[36:37], v[38:39]
	v_pk_mul_f32 v[30:31], s[0:1], v[30:31] op_sel_hi:[0,1]
	v_pk_fma_f32 v[32:33], v[40:41], v[36:37], v[32:33] neg_lo:[1,0,0] neg_hi:[1,0,0]
	v_pk_fma_f32 v[30:31], v[30:31], v[238:239], v[242:243]
	v_cvt_pk_f16_f32 v34, v34, v35
	v_cvt_pk_f16_f32 v35, v32, v33
	v_fma_f32 v13, |v30|, s25, 1.0
	ds_write_b64 v137, v[34:35] offset:37888
	v_rcp_f32_e32 v34, v13
	v_fma_f32 v13, |v31|, s25, 1.0
	v_rcp_f32_e32 v35, v13
	v_pk_mul_f32 v[36:37], v[30:31], v[30:31]
	v_pk_mul_f32 v[28:29], s[0:1], v[28:29] op_sel_hi:[0,1]
	v_mul_f32_e32 v13, 0xbf38aa3b, v36
	v_pk_fma_f32 v[38:39], v[34:35], s[22:23], v[90:91] op_sel_hi:[1,0,0]
	v_exp_f32_e32 v36, v13
	v_pk_fma_f32 v[38:39], v[34:35], v[38:39], s[24:25] op_sel_hi:[1,1,0]
	v_mul_f32_e32 v13, 0xbf38aa3b, v37
	v_pk_fma_f32 v[38:39], v[34:35], v[38:39], s[34:35] op_sel_hi:[1,1,0]
	v_pk_fma_f32 v[28:29], v[28:29], v[240:241], v[244:245]
	v_pk_fma_f32 v[38:39], v[34:35], v[38:39], s[40:41] op_sel_hi:[1,1,0]
	v_and_b32_e32 v33, 0x7fffffff, v31
	v_and_b32_e32 v32, 0x7fffffff, v30
	v_exp_f32_e32 v37, v13
	v_pk_mul_f32 v[34:35], v[34:35], v[38:39]
	v_fma_f32 v13, |v28|, s25, 1.0
	v_pk_mul_f32 v[32:33], v[32:33], v[34:35]
	v_rcp_f32_e32 v34, v13
	v_fma_f32 v13, |v29|, s25, 1.0
	v_rcp_f32_e32 v35, v13
	v_max_f32_e32 v30, 0, v30
	v_max_f32_e32 v31, 0, v31
	v_pk_fma_f32 v[30:31], v[36:37], v[32:33], v[30:31] neg_lo:[1,0,0] neg_hi:[1,0,0]
	v_pk_mul_f32 v[36:37], v[28:29], v[28:29]
	v_pk_fma_f32 v[38:39], v[34:35], s[22:23], v[90:91] op_sel_hi:[1,0,0]
	v_mul_f32_e32 v13, 0xbf38aa3b, v36
	v_exp_f32_e32 v36, v13
	v_pk_fma_f32 v[38:39], v[34:35], v[38:39], s[24:25] op_sel_hi:[1,1,0]
	v_mul_f32_e32 v13, 0xbf38aa3b, v37
	v_pk_fma_f32 v[38:39], v[34:35], v[38:39], s[34:35] op_sel_hi:[1,1,0]
	v_exp_f32_e32 v37, v13
	v_pk_fma_f32 v[38:39], v[34:35], v[38:39], s[40:41] op_sel_hi:[1,1,0]
	v_and_b32_e32 v33, 0x7fffffff, v29
	v_and_b32_e32 v32, 0x7fffffff, v28
	v_pk_mul_f32 v[34:35], v[34:35], v[38:39]
	v_readlane_b32 s0, v12, 4
	v_max_f32_e32 v28, 0, v28
	v_max_f32_e32 v29, 0, v29
	v_pk_mul_f32 v[32:33], v[32:33], v[34:35]
	v_pk_mul_f32 v[26:27], s[0:1], v[26:27] op_sel_hi:[0,1]
	v_pk_fma_f32 v[28:29], v[36:37], v[32:33], v[28:29] neg_lo:[1,0,0] neg_hi:[1,0,0]
	v_pk_fma_f32 v[26:27], v[26:27], v[238:239], v[242:243]
	v_cvt_pk_f16_f32 v30, v30, v31
	v_cvt_pk_f16_f32 v31, v28, v29
	v_fma_f32 v13, |v26|, s25, 1.0
	ds_write_b64 v136, v[30:31] offset:38400
	v_rcp_f32_e32 v30, v13
	v_fma_f32 v13, |v27|, s25, 1.0
	v_rcp_f32_e32 v31, v13
	v_pk_mul_f32 v[32:33], v[26:27], v[26:27]
	v_pk_mul_f32 v[24:25], s[0:1], v[24:25] op_sel_hi:[0,1]
	v_mul_f32_e32 v13, 0xbf38aa3b, v32
	v_pk_fma_f32 v[34:35], v[30:31], s[22:23], v[90:91] op_sel_hi:[1,0,0]
	v_exp_f32_e32 v32, v13
	v_pk_fma_f32 v[34:35], v[30:31], v[34:35], s[24:25] op_sel_hi:[1,1,0]
	v_mul_f32_e32 v13, 0xbf38aa3b, v33
	v_pk_fma_f32 v[34:35], v[30:31], v[34:35], s[34:35] op_sel_hi:[1,1,0]
	v_pk_fma_f32 v[24:25], v[24:25], v[240:241], v[244:245]
	v_pk_fma_f32 v[34:35], v[30:31], v[34:35], s[40:41] op_sel_hi:[1,1,0]
	v_and_b32_e32 v29, 0x7fffffff, v27
	v_and_b32_e32 v28, 0x7fffffff, v26
	v_exp_f32_e32 v33, v13
	v_pk_mul_f32 v[30:31], v[30:31], v[34:35]
	v_fma_f32 v13, |v24|, s25, 1.0
	v_pk_mul_f32 v[28:29], v[28:29], v[30:31]
	v_rcp_f32_e32 v30, v13
	v_fma_f32 v13, |v25|, s25, 1.0
	v_rcp_f32_e32 v31, v13
	v_max_f32_e32 v26, 0, v26
	v_max_f32_e32 v27, 0, v27
	v_pk_fma_f32 v[26:27], v[32:33], v[28:29], v[26:27] neg_lo:[1,0,0] neg_hi:[1,0,0]
	v_pk_mul_f32 v[32:33], v[24:25], v[24:25]
	v_pk_fma_f32 v[34:35], v[30:31], s[22:23], v[90:91] op_sel_hi:[1,0,0]
	v_mul_f32_e32 v13, 0xbf38aa3b, v32
	v_exp_f32_e32 v32, v13
	v_pk_fma_f32 v[34:35], v[30:31], v[34:35], s[24:25] op_sel_hi:[1,1,0]
	v_mul_f32_e32 v13, 0xbf38aa3b, v33
	v_pk_fma_f32 v[34:35], v[30:31], v[34:35], s[34:35] op_sel_hi:[1,1,0]
	v_exp_f32_e32 v33, v13
	v_pk_fma_f32 v[34:35], v[30:31], v[34:35], s[40:41] op_sel_hi:[1,1,0]
	v_and_b32_e32 v29, 0x7fffffff, v25
	v_and_b32_e32 v28, 0x7fffffff, v24
	v_pk_mul_f32 v[30:31], v[30:31], v[34:35]
	v_readlane_b32 s0, v12, 5
	v_max_f32_e32 v24, 0, v24
	v_max_f32_e32 v25, 0, v25
	v_pk_mul_f32 v[28:29], v[28:29], v[30:31]
	v_pk_mul_f32 v[22:23], s[0:1], v[22:23] op_sel_hi:[0,1]
	v_pk_fma_f32 v[24:25], v[32:33], v[28:29], v[24:25] neg_lo:[1,0,0] neg_hi:[1,0,0]
	v_pk_fma_f32 v[22:23], v[22:23], v[238:239], v[242:243]
	v_cvt_pk_f16_f32 v26, v26, v27
	v_cvt_pk_f16_f32 v27, v24, v25
	v_fma_f32 v13, |v22|, s25, 1.0
	ds_write_b64 v123, v[26:27] offset:38912
	v_rcp_f32_e32 v26, v13
	v_fma_f32 v13, |v23|, s25, 1.0
	v_rcp_f32_e32 v27, v13
	v_pk_mul_f32 v[28:29], v[22:23], v[22:23]
	v_pk_mul_f32 v[20:21], s[0:1], v[20:21] op_sel_hi:[0,1]
	v_mul_f32_e32 v13, 0xbf38aa3b, v28
	v_pk_fma_f32 v[30:31], v[26:27], s[22:23], v[90:91] op_sel_hi:[1,0,0]
	v_exp_f32_e32 v28, v13
	v_pk_fma_f32 v[30:31], v[26:27], v[30:31], s[24:25] op_sel_hi:[1,1,0]
	v_mul_f32_e32 v13, 0xbf38aa3b, v29
	v_pk_fma_f32 v[30:31], v[26:27], v[30:31], s[34:35] op_sel_hi:[1,1,0]
	v_pk_fma_f32 v[20:21], v[20:21], v[240:241], v[244:245]
	v_pk_fma_f32 v[30:31], v[26:27], v[30:31], s[40:41] op_sel_hi:[1,1,0]
	s_waitcnt vmcnt(7)
	v_add_f32_e32 v92, v170, v171
	v_add_f32_e32 v93, v172, v173
	v_and_b32_e32 v25, 0x7fffffff, v23
	v_and_b32_e32 v24, 0x7fffffff, v22
	v_exp_f32_e32 v29, v13
	v_pk_mul_f32 v[26:27], v[26:27], v[30:31]
	v_fma_f32 v13, |v20|, s25, 1.0
	v_add_f32_e32 v92, v92, v93
	s_waitcnt vmcnt(6)
	v_add_f32_e32 v93, v174, v175
	v_add_f32_e32 v94, v176, v177
	v_pk_mul_f32 v[24:25], v[24:25], v[26:27]
	v_rcp_f32_e32 v26, v13
	v_fma_f32 v13, |v21|, s25, 1.0
	v_add_f32_e32 v93, v93, v94
	s_waitcnt vmcnt(5)
	v_add_f32_e32 v94, v178, v179
	v_add_f32_e32 v95, v180, v181
	v_rcp_f32_e32 v27, v13
	v_add_f32_e32 v94, v94, v95
	s_waitcnt vmcnt(4)
	v_add_f32_e32 v95, v182, v183
	v_add_f32_e32 v96, v184, v185
	v_add_f32_e32 v95, v95, v96
	s_waitcnt vmcnt(3)
	v_add_f32_e32 v96, v186, v187
	v_add_f32_e32 v97, v188, v189
	v_max_f32_e32 v22, 0, v22
	v_max_f32_e32 v23, 0, v23
	v_add_f32_e32 v96, v96, v97
	s_waitcnt vmcnt(2)
	v_add_f32_e32 v97, v190, v191
	v_add_f32_e32 v98, v192, v193
	v_pk_fma_f32 v[22:23], v[28:29], v[24:25], v[22:23] neg_lo:[1,0,0] neg_hi:[1,0,0]
	v_pk_mul_f32 v[28:29], v[20:21], v[20:21]
	v_add_f32_e32 v97, v97, v98
	s_waitcnt vmcnt(1)
	v_add_f32_e32 v98, v194, v195
	v_add_f32_e32 v99, v196, v197
	v_mul_f32_e32 v13, 0xbf38aa3b, v28
	v_pk_fma_f32 v[30:31], v[26:27], s[22:23], v[90:91] op_sel_hi:[1,0,0]
	v_add_f32_e32 v98, v98, v99
	s_waitcnt vmcnt(0)
	v_add_f32_e32 v99, v198, v199
	v_add_f32_e32 v100, v200, v201
	v_exp_f32_e32 v28, v13
	v_pk_fma_f32 v[30:31], v[26:27], v[30:31], s[24:25] op_sel_hi:[1,1,0]
	v_mul_f32_e32 v13, 0xbf38aa3b, v29
	v_add_f32_e32 v99, v99, v100
	v_cndmask_b32_e64 v100, v93, v92, s[4:5]
	v_cndmask_b32_e64 v92, v92, v93, s[4:5]
	v_cndmask_b32_e64 v93, v95, v94, s[4:5]
	v_cndmask_b32_e64 v94, v94, v95, s[4:5]
	v_pk_fma_f32 v[30:31], v[26:27], v[30:31], s[34:35] op_sel_hi:[1,1,0]
	v_exp_f32_e32 v29, v13
	v_add_f32_dpp v93, v93, v94 quad_perm:[1,0,3,2] row_mask:0xf bank_mask:0xf bound_ctrl:1
	v_cndmask_b32_e64 v94, v97, v96, s[4:5]
	v_cndmask_b32_e64 v95, v96, v97, s[4:5]
	v_pk_fma_f32 v[30:31], v[26:27], v[30:31], s[40:41] op_sel_hi:[1,1,0]
	v_cndmask_b32_e64 v96, v98, v99, s[4:5]
	v_add_f32_dpp v94, v94, v95 quad_perm:[1,0,3,2] row_mask:0xf bank_mask:0xf bound_ctrl:1
	v_cndmask_b32_e64 v95, v99, v98, s[4:5]
	v_and_b32_e32 v25, 0x7fffffff, v21
	v_and_b32_e32 v24, 0x7fffffff, v20
	v_pk_mul_f32 v[26:27], v[26:27], v[30:31]
	v_readlane_b32 s0, v12, 6
	v_add_f32_dpp v92, v100, v92 quad_perm:[1,0,3,2] row_mask:0xf bank_mask:0xf bound_ctrl:1
	v_add_f32_dpp v95, v95, v96 quad_perm:[1,0,3,2] row_mask:0xf bank_mask:0xf bound_ctrl:1
	v_max_f32_e32 v20, 0, v20
	v_max_f32_e32 v21, 0, v21
	v_pk_mul_f32 v[24:25], v[24:25], v[26:27]
	v_pk_mul_f32 v[18:19], s[0:1], v[18:19] op_sel_hi:[0,1]
	v_cndmask_b32_e64 v96, v92, v93, s[6:7]
	v_cndmask_b32_e64 v92, v93, v92, s[6:7]
	v_cndmask_b32_e64 v93, v94, v95, s[6:7]
	v_cndmask_b32_e64 v94, v95, v94, s[6:7]
	v_pk_fma_f32 v[20:21], v[28:29], v[24:25], v[20:21] neg_lo:[1,0,0] neg_hi:[1,0,0]
	v_pk_fma_f32 v[18:19], v[18:19], v[238:239], v[242:243]
	v_add_f32_dpp v92, v96, v92 quad_perm:[2,3,0,1] row_mask:0xf bank_mask:0xf bound_ctrl:1
	v_add_f32_dpp v93, v93, v94 quad_perm:[2,3,0,1] row_mask:0xf bank_mask:0xf bound_ctrl:1
	v_cvt_pk_f16_f32 v22, v22, v23
	v_cvt_pk_f16_f32 v23, v20, v21
	v_fma_f32 v13, |v18|, s25, 1.0
	v_cndmask_b32_e64 v94, v92, v93, s[8:9]
	ds_write_b64 v133, v[22:23] offset:39424
	v_rcp_f32_e32 v22, v13
	v_fma_f32 v13, |v19|, s25, 1.0
	v_cndmask_b32_e64 v92, v93, v92, s[8:9]
	v_mov_b32_e32 v93, v94
	v_rcp_f32_e32 v23, v13
	v_pk_mul_f32 v[24:25], v[18:19], v[18:19]
	v_mov_b32_dpp v93, v93 row_shl:4 row_mask:0xf bank_mask:0x5
	v_mul_f32_e32 v13, 0xbf38aa3b, v24
	v_pk_fma_f32 v[26:27], v[22:23], s[22:23], v[90:91] op_sel_hi:[1,0,0]
	v_mov_b32_dpp v93, v94 row_shr:4 row_mask:0xf bank_mask:0xa
	v_add_f32_e32 v92, v92, v93
	v_pk_fma_f32 v[26:27], v[22:23], v[26:27], s[24:25] op_sel_hi:[1,1,0]
	v_pk_mul_f32 v[16:17], s[0:1], v[16:17] op_sel_hi:[0,1]
	v_add_f32_dpp v92, v92, v92 row_ror:8 row_mask:0xf bank_mask:0xf bound_ctrl:1
	v_mov_b32_e32 v93, v92
	s_nop 1
	v_permlane16_swap_b32_e32 v92, v93
	v_pk_fma_f32 v[26:27], v[22:23], v[26:27], s[34:35] op_sel_hi:[1,1,0]
	v_add_f32_e32 v92, v92, v93
	v_exp_f32_e32 v24, v13
	v_pk_fma_f32 v[26:27], v[22:23], v[26:27], s[40:41] op_sel_hi:[1,1,0]
	v_mul_f32_e32 v13, 0xbf38aa3b, v25
	v_pk_fma_f32 v[16:17], v[16:17], v[240:241], v[244:245]
	v_mov_b32_e32 v93, v92
	v_and_b32_e32 v21, 0x7fffffff, v19
	v_and_b32_e32 v20, 0x7fffffff, v18
	v_exp_f32_e32 v25, v13
	v_pk_mul_f32 v[22:23], v[22:23], v[26:27]
	v_fma_f32 v13, |v16|, s25, 1.0
	v_permlane32_swap_b32_e32 v92, v93
	v_pk_mul_f32 v[20:21], v[20:21], v[22:23]
	v_rcp_f32_e32 v22, v13
	v_fma_f32 v13, |v17|, s25, 1.0
	v_add_f32_e32 v92, v92, v93
	v_rcp_f32_e32 v23, v13
	v_mul_f32_e32 v92, 0x3b800000, v92
	v_max_f32_e32 v18, 0, v18
	v_max_f32_e32 v19, 0, v19
	v_readlane_b32 s42, v92, 0
	v_readlane_b32 s44, v92, 1
	v_readlane_b32 s46, v92, 2
	v_readlane_b32 s48, v92, 3
	v_pk_fma_f32 v[18:19], v[24:25], v[20:21], v[18:19] neg_lo:[1,0,0] neg_hi:[1,0,0]
	v_pk_mul_f32 v[24:25], v[16:17], v[16:17]
	v_pk_add_f32 v[160:161], v[172:173], s[42:43] op_sel_hi:[1, 0] neg_lo:[0, 1] neg_hi:[0, 1]
	v_pk_add_f32 v[110:111], v[176:177], s[44:45] op_sel_hi:[1, 0] neg_lo:[0, 1] neg_hi:[0, 1]
	v_pk_add_f32 v[104:105], v[180:181], s[46:47] op_sel_hi:[1, 0] neg_lo:[0, 1] neg_hi:[0, 1]
	v_pk_add_f32 v[100:101], v[184:185], s[48:49] op_sel_hi:[1, 0] neg_lo:[0, 1] neg_hi:[0, 1]
	v_mul_f32_e32 v13, 0xbf38aa3b, v24
	v_pk_add_f32 v[158:159], v[170:171], s[42:43] op_sel_hi:[1, 0] neg_lo:[0, 1] neg_hi:[0, 1]
	v_mul_f32_e32 v78, v161, v161
	v_pk_add_f32 v[162:163], v[174:175], s[44:45] op_sel_hi:[1, 0] neg_lo:[0, 1] neg_hi:[0, 1]
	v_mul_f32_e32 v74, v111, v111
	v_pk_add_f32 v[108:109], v[178:179], s[46:47] op_sel_hi:[1, 0] neg_lo:[0, 1] neg_hi:[0, 1]
	v_mul_f32_e32 v70, v105, v105
	v_pk_add_f32 v[102:103], v[182:183], s[48:49] op_sel_hi:[1, 0] neg_lo:[0, 1] neg_hi:[0, 1]
	v_mul_f32_e32 v66, v101, v101
	v_exp_f32_e32 v24, v13
	v_pk_fma_f32 v[26:27], v[22:23], s[22:23], v[90:91] op_sel_hi:[1,0,0]
	v_mul_f32_e32 v13, 0xbf38aa3b, v25
	v_readlane_b32 s0, v12, 7
	v_fmac_f32_e32 v78, v160, v160
	v_fmac_f32_e32 v74, v110, v110
	v_fmac_f32_e32 v70, v104, v104
	v_fmac_f32_e32 v66, v100, v100
	v_pk_fma_f32 v[26:27], v[22:23], v[26:27], s[24:25] op_sel_hi:[1,1,0]
	v_exp_f32_e32 v25, v13
	v_pk_mul_f32 v[12:13], s[0:1], v[14:15] op_sel_hi:[0,1]
	v_pk_mul_f32 v[10:11], s[0:1], v[10:11] op_sel_hi:[0,1]
	s_movk_i32 s0, 0x6000
	v_fmac_f32_e32 v78, v159, v159
	v_fmac_f32_e32 v74, v163, v163
	v_fmac_f32_e32 v70, v109, v109
	v_fmac_f32_e32 v66, v103, v103
	v_pk_fma_f32 v[26:27], v[22:23], v[26:27], s[34:35] op_sel_hi:[1,1,0]
	v_add_co_u32_e32 v154, vcc, s0, v82
	v_fmac_f32_e32 v78, v158, v158
	v_fmac_f32_e32 v74, v162, v162
	v_fmac_f32_e32 v70, v108, v108
	v_fmac_f32_e32 v66, v102, v102
	v_pk_fma_f32 v[26:27], v[22:23], v[26:27], s[40:41] op_sel_hi:[1,1,0]
	v_addc_co_u32_e32 v155, vcc, 0, v83, vcc
	s_movk_i32 s0, 0x7000
	v_cndmask_b32_e64 v75, v74, v78, s[4:5]
	v_cndmask_b32_e64 v74, v78, v74, s[4:5]
	v_cndmask_b32_e64 v67, v66, v70, s[4:5]
	v_cndmask_b32_e64 v66, v70, v66, s[4:5]
	v_and_b32_e32 v21, 0x7fffffff, v17
	v_and_b32_e32 v20, 0x7fffffff, v16
	v_pk_mul_f32 v[22:23], v[22:23], v[26:27]
	v_add_co_u32_e32 v156, vcc, s0, v82
	v_readlane_b32 s50, v92, 4
	v_readlane_b32 s52, v92, 5
	v_readlane_b32 s54, v92, 6
	v_readlane_b32 s0, v92, 7
	v_add_f32_dpp v74, v75, v74 quad_perm:[1,0,3,2] row_mask:0xf bank_mask:0xf bound_ctrl:1
	v_add_f32_dpp v66, v67, v66 quad_perm:[1,0,3,2] row_mask:0xf bank_mask:0xf bound_ctrl:1
	v_max_f32_e32 v16, 0, v16
	v_max_f32_e32 v17, 0, v17
	v_pk_mul_f32 v[20:21], v[20:21], v[22:23]
	v_cndmask_b32_e64 v67, v74, v66, s[6:7]
	v_cndmask_b32_e64 v66, v66, v74, s[6:7]
	v_pk_add_f32 v[96:97], v[188:189], s[50:51] op_sel_hi:[1, 0] neg_lo:[0, 1] neg_hi:[0, 1]
	v_pk_add_f32 v[92:93], v[192:193], s[52:53] op_sel_hi:[1, 0] neg_lo:[0, 1] neg_hi:[0, 1]
	v_pk_add_f32 v[78:79], v[196:197], s[54:55] op_sel_hi:[1, 0] neg_lo:[0, 1] neg_hi:[0, 1]
	v_pk_add_f32 v[74:75], v[200:201], s[0:1] op_sel_hi:[1, 0] neg_lo:[0, 1] neg_hi:[0, 1]
	v_pk_fma_f32 v[16:17], v[24:25], v[20:21], v[16:17] neg_lo:[1,0,0] neg_hi:[1,0,0]
	v_pk_fma_f32 v[12:13], v[12:13], v[238:239], v[242:243]
	v_pk_add_f32 v[98:99], v[186:187], s[50:51] op_sel_hi:[1, 0] neg_lo:[0, 1] neg_hi:[0, 1]
	v_mul_f32_e32 v62, v97, v97
	v_pk_add_f32 v[94:95], v[190:191], s[52:53] op_sel_hi:[1, 0] neg_lo:[0, 1] neg_hi:[0, 1]
	v_mul_f32_e32 v58, v93, v93
	v_pk_add_f32 v[80:81], v[194:195], s[54:55] op_sel_hi:[1, 0] neg_lo:[0, 1] neg_hi:[0, 1]
	v_mul_f32_e32 v54, v79, v79
	v_pk_add_f32 v[76:77], v[198:199], s[0:1] op_sel_hi:[1, 0] neg_lo:[0, 1] neg_hi:[0, 1]
	v_mul_f32_e32 v50, v75, v75
	v_cvt_pk_f16_f32 v18, v18, v19
	v_cvt_pk_f16_f32 v19, v16, v17
	v_fma_f32 v16, |v12|, s25, 1.0
	v_fma_f32 v17, |v13|, s25, 1.0
	v_fmac_f32_e32 v62, v96, v96
	v_fmac_f32_e32 v58, v92, v92
	v_fmac_f32_e32 v54, v78, v78
	v_fmac_f32_e32 v50, v74, v74
	v_rcp_f32_e32 v16, v16
	v_rcp_f32_e32 v17, v17
	v_fmac_f32_e32 v62, v99, v99
	v_fmac_f32_e32 v58, v95, v95
	v_fmac_f32_e32 v54, v81, v81
	v_fmac_f32_e32 v50, v77, v77
	v_fmac_f32_e32 v62, v98, v98
	v_fmac_f32_e32 v58, v94, v94
	v_fmac_f32_e32 v54, v80, v80
	v_fmac_f32_e32 v50, v76, v76
	v_cndmask_b32_e64 v59, v58, v62, s[4:5]
	v_cndmask_b32_e64 v58, v62, v58, s[4:5]
	v_cndmask_b32_e64 v51, v50, v54, s[4:5]
	v_cndmask_b32_e64 v50, v54, v50, s[4:5]
	v_add_f32_dpp v58, v59, v58 quad_perm:[1,0,3,2] row_mask:0xf bank_mask:0xf bound_ctrl:1
	ds_write_b64 v119, v[18:19] offset:39936
	v_add_f32_dpp v50, v51, v50 quad_perm:[1,0,3,2] row_mask:0xf bank_mask:0xf bound_ctrl:1
	v_pk_mul_f32 v[18:19], v[12:13], v[12:13]
	v_pk_fma_f32 v[20:21], v[16:17], s[22:23], v[90:91] op_sel_hi:[1,0,0]
	v_cndmask_b32_e64 v51, v58, v50, s[6:7]
	v_cndmask_b32_e64 v50, v50, v58, s[6:7]
	v_mul_f32_e32 v18, 0xbf38aa3b, v18
	v_pk_fma_f32 v[20:21], v[16:17], v[20:21], s[24:25] op_sel_hi:[1,1,0]
	v_mul_f32_e32 v19, 0xbf38aa3b, v19
	v_add_f32_dpp v66, v67, v66 quad_perm:[2,3,0,1] row_mask:0xf bank_mask:0xf bound_ctrl:1
	v_add_f32_dpp v50, v51, v50 quad_perm:[2,3,0,1] row_mask:0xf bank_mask:0xf bound_ctrl:1
	v_exp_f32_e32 v18, v18
	v_pk_fma_f32 v[20:21], v[16:17], v[20:21], s[34:35] op_sel_hi:[1,1,0]
	v_exp_f32_e32 v19, v19
	v_cndmask_b32_e64 v51, v66, v50, s[8:9]
	v_pk_fma_f32 v[20:21], v[16:17], v[20:21], s[40:41] op_sel_hi:[1,1,0]
	v_mov_b32_e32 v52, v51
	v_and_b32_e32 v15, 0x7fffffff, v13
	v_and_b32_e32 v14, 0x7fffffff, v12
	v_pk_mul_f32 v[16:17], v[16:17], v[20:21]
	v_mov_b32_dpp v52, v52 row_shl:4 row_mask:0xf bank_mask:0x5
	v_max_f32_e32 v12, 0, v12
	v_max_f32_e32 v13, 0, v13
	v_pk_mul_f32 v[14:15], v[14:15], v[16:17]
	v_cndmask_b32_e64 v50, v50, v66, s[8:9]
	v_mov_b32_dpp v52, v51 row_shr:4 row_mask:0xf bank_mask:0xa
	v_pk_fma_f32 v[12:13], v[18:19], v[14:15], v[12:13] neg_lo:[1,0,0] neg_hi:[1,0,0]
	v_pk_fma_f32 v[10:11], v[10:11], v[240:241], v[244:245]
	v_add_f32_e32 v50, v50, v52
	v_cvt_pk_f16_f32 v12, v12, v13
	v_fma_f32 v13, |v10|, s25, 1.0
	v_add_f32_dpp v50, v50, v50 row_ror:8 row_mask:0xf bank_mask:0xf bound_ctrl:1
	v_rcp_f32_e32 v16, v13
	v_fma_f32 v13, |v11|, s25, 1.0
	v_mov_b32_e32 v51, v50
	v_rcp_f32_e32 v17, v13
	s_nop 0
	v_permlane16_swap_b32_e32 v50, v51
	v_add_f32_e32 v50, v50, v51
	v_mov_b32_e32 v51, v50
	v_pk_mul_f32 v[18:19], v[10:11], v[10:11]
	s_nop 0
	v_permlane32_swap_b32_e32 v50, v51
	v_mul_f32_e32 v13, 0xbf38aa3b, v18
	v_pk_fma_f32 v[20:21], v[16:17], s[22:23], v[90:91] op_sel_hi:[1,0,0]
	v_add_f32_e32 v50, v50, v51
	v_exp_f32_e32 v18, v13
	v_pk_fma_f32 v[20:21], v[16:17], v[20:21], s[24:25] op_sel_hi:[1,1,0]
	v_mul_f32_e32 v13, 0xbf38aa3b, v19
	v_addc_co_u32_e32 v157, vcc, 0, v83, vcc
	v_fmamk_f32 v50, v50, 0x3b800000, v116
	v_pk_fma_f32 v[20:21], v[16:17], v[20:21], s[34:35] op_sel_hi:[1,1,0]
	v_exp_f32_e32 v19, v13
	v_mul_f32_e32 v51, 0x4f800000, v50
	v_cmp_gt_f32_e32 vcc, s35, v50
	v_pk_fma_f32 v[20:21], v[16:17], v[20:21], s[40:41] op_sel_hi:[1,1,0]
	v_and_b32_e32 v15, 0x7fffffff, v11
	v_cndmask_b32_e32 v50, v50, v51, vcc
	v_and_b32_e32 v14, 0x7fffffff, v10
	v_pk_mul_f32 v[16:17], v[16:17], v[20:21]
	v_sqrt_f32_e32 v51, v50
	v_max_f32_e32 v10, 0, v10
	v_max_f32_e32 v11, 0, v11
	v_pk_mul_f32 v[14:15], v[14:15], v[16:17]
	v_add_u32_e32 v52, -1, v51
	v_pk_fma_f32 v[10:11], v[18:19], v[14:15], v[10:11] neg_lo:[1,0,0] neg_hi:[1,0,0]
	v_fma_f32 v53, -v52, v51, v50
	v_cvt_pk_f16_f32 v13, v10, v11
	v_bitop3_b32 v10, v86, s41, v88 bitop3:0x6c
	v_or3_b32 v146, v85, v10, v87
	v_lshlrev_b32_e32 v10, 4, v141
	v_and_or_b32 v147, v10, s41, v84
	v_lshlrev_b32_e32 v10, 4, v142
	v_and_or_b32 v148, v10, s41, v84
	v_lshlrev_b32_e32 v10, 4, v143
	v_cmp_ge_f32_e64 s[0:1], 0, v53
	v_add_u32_e32 v53, 1, v51
	v_and_or_b32 v149, v10, s41, v84
	v_bitop3_b32 v10, v125, v0, 15 bitop3:0x78
	v_cndmask_b32_e64 v52, v51, v52, s[0:1]
	v_fma_f32 v51, -v53, v51, v50
	v_lshl_or_b32 v150, v10, 4, v84
	v_bitop3_b32 v10, v125, v107, 4 bitop3:0x36
	v_cmp_lt_f32_e64 s[0:1], 0, v51
	v_lshl_or_b32 v151, v10, 4, v84
	v_bitop3_b32 v10, v125, v107, 8 bitop3:0x36
	v_cndmask_b32_e64 v51, v52, v53, s[0:1]
	v_lshl_or_b32 v152, v10, 4, v84
	v_bitop3_b32 v10, v125, v107, 12 bitop3:0x36
	v_mul_f32_e32 v52, 0x37800000, v51
	ds_write_b64 v146, v[12:13] offset:40448
	v_lshl_or_b32 v153, v10, 4, v84
	v_cndmask_b32_e32 v51, v51, v52, vcc
	v_cmp_class_f32_e32 vcc, v50, v117
	ds_read_b128 v[38:41], v115 offset:32768
	ds_read_b128 v[34:37], v147 offset:32768
	ds_read_b128 v[30:33], v148 offset:32768
	ds_read_b128 v[26:29], v149 offset:32768
	ds_read_b128 v[22:25], v150 offset:33024
	ds_read_b128 v[18:21], v151 offset:33024
	ds_read_b128 v[14:17], v152 offset:33024
	ds_read_b128 v[10:13], v153 offset:33024
	s_movk_i32 s57, 0x7000
	s_nop 1
	v_add_co_u32_e64 v236, s[60:61], s57, v82
	s_nop 1
	v_addc_co_u32_e64 v237, s[60:61], 0, v83, s[60:61]
	s_nop 1
	global_load_dwordx4 v[206:209], v[236:237], off offset:-3072 nt
	global_load_dwordx4 v[210:213], v[236:237], off offset:-2048 nt
	global_load_dwordx4 v[214:217], v[236:237], off offset:-1024 nt
	global_load_dwordx4 v[202:205], v[236:237], off offset:-4096 nt
	global_load_dwordx4 v[218:221], v[236:237], off nt
	v_cndmask_b32_e32 v154, v51, v50, vcc
	v_div_scale_f32 v155, s[0:1], v154, v154, 1.0
	v_rcp_f32_e32 v164, v155
	global_load_dwordx4 v[222:225], v[236:237], off offset:1024 nt
	global_load_dwordx4 v[226:229], v[236:237], off offset:2048 nt
	global_load_dwordx4 v[230:233], v[236:237], off offset:3072 nt
	s_lshr_b32 s60, s2, 3
	s_lshl_b32 s60, s60, 16
	s_add_u32 s60, s36, s60
	s_addc_u32 s61, s37, 0
	v_lshlrev_b32_e32 v234, 7, v0
	global_load_dword v246, v234, s[60:61] sc1
	v_fma_f32 v156, -v155, v164, 1.0
	v_fmac_f32_e32 v164, v156, v164
	v_div_scale_f32 v156, vcc, 1.0, v154, 1.0
	v_mul_f32_e32 v157, v156, v164
	v_fma_f32 v165, -v155, v157, v156
	v_fmac_f32_e32 v157, v165, v164
	v_fma_f32 v155, -v155, v157, v156
	v_div_fmas_f32 v155, v155, v164, v157
	v_div_fixup_f32 v154, v155, v154, 1.0
	s_nop 0
	v_readlane_b32 s0, v154, 0
	s_nop 1
	v_pk_mul_f32 v[156:157], s[0:1], v[158:159] op_sel_hi:[0,1]
	v_pk_fma_f32 v[156:157], v[156:157], v[238:239], v[242:243]
	s_nop 0
	v_fma_f32 v155, |v156|, s25, 1.0
	v_rcp_f32_e32 v164, v155
	v_fma_f32 v155, |v157|, s25, 1.0
	v_rcp_f32_e32 v165, v155
	v_pk_mul_f32 v[166:167], v[156:157], v[156:157]
	v_and_b32_e32 v159, 0x7fffffff, v157
	v_mul_f32_e32 v155, 0xbf38aa3b, v166
	v_pk_fma_f32 v[168:169], v[164:165], s[22:23], v[90:91] op_sel_hi:[1,0,0]
	v_exp_f32_e32 v166, v155
	v_pk_fma_f32 v[168:169], v[164:165], v[168:169], s[24:25] op_sel_hi:[1,1,0]
	v_mul_f32_e32 v155, 0xbf38aa3b, v167
	v_pk_fma_f32 v[168:169], v[164:165], v[168:169], s[34:35] op_sel_hi:[1,1,0]
	v_exp_f32_e32 v167, v155
	v_pk_fma_f32 v[168:169], v[164:165], v[168:169], s[40:41] op_sel_hi:[1,1,0]
	v_and_b32_e32 v158, 0x7fffffff, v156
	v_pk_mul_f32 v[164:165], v[164:165], v[168:169]
	v_max_f32_e32 v156, 0, v156
	v_max_f32_e32 v157, 0, v157
	v_pk_mul_f32 v[158:159], v[158:159], v[164:165]
	s_nop 0
	v_pk_fma_f32 v[156:157], v[166:167], v[158:159], v[156:157] neg_lo:[1,0,0] neg_hi:[1,0,0]
	v_pk_mul_f32 v[158:159], s[0:1], v[160:161] op_sel_hi:[0,1]
	v_pk_fma_f32 v[158:159], v[158:159], v[240:241], v[244:245]
	v_cvt_pk_f16_f32 v156, v156, v157
	v_fma_f32 v155, |v158|, s25, 1.0
	v_rcp_f32_e32 v164, v155
	v_fma_f32 v155, |v159|, s25, 1.0
	v_rcp_f32_e32 v165, v155
	v_pk_mul_f32 v[166:167], v[158:159], v[158:159]
	v_and_b32_e32 v161, 0x7fffffff, v159
	v_mul_f32_e32 v155, 0xbf38aa3b, v166
	v_pk_fma_f32 v[168:169], v[164:165], s[22:23], v[90:91] op_sel_hi:[1,0,0]
	v_exp_f32_e32 v166, v155
	v_pk_fma_f32 v[168:169], v[164:165], v[168:169], s[24:25] op_sel_hi:[1,1,0]
	v_mul_f32_e32 v155, 0xbf38aa3b, v167
	v_pk_fma_f32 v[168:169], v[164:165], v[168:169], s[34:35] op_sel_hi:[1,1,0]
	v_exp_f32_e32 v167, v155
	v_pk_fma_f32 v[168:169], v[164:165], v[168:169], s[40:41] op_sel_hi:[1,1,0]
	v_and_b32_e32 v160, 0x7fffffff, v158
	v_pk_mul_f32 v[164:165], v[164:165], v[168:169]
	v_max_f32_e32 v158, 0, v158
	v_max_f32_e32 v159, 0, v159
	v_pk_mul_f32 v[160:161], v[160:161], v[164:165]
	v_readlane_b32 s0, v154, 1
	v_pk_fma_f32 v[158:159], v[166:167], v[160:161], v[158:159] neg_lo:[1,0,0] neg_hi:[1,0,0]
	s_nop 0
	v_cvt_pk_f16_f32 v157, v158, v159
	ds_write_b64 v140, v[156:157] offset:32768
	v_pk_mul_f32 v[156:157], s[0:1], v[162:163] op_sel_hi:[0,1]
	v_pk_fma_f32 v[156:157], v[156:157], v[238:239], v[242:243]
	v_pk_mul_f32 v[110:111], s[0:1], v[110:111] op_sel_hi:[0,1]
	v_fma_f32 v140, |v156|, s25, 1.0
	v_rcp_f32_e32 v160, v140
	v_fma_f32 v140, |v157|, s25, 1.0
	v_rcp_f32_e32 v161, v140
	v_pk_mul_f32 v[162:163], v[156:157], v[156:157]
	v_pk_fma_f32 v[110:111], v[110:111], v[240:241], v[244:245]
	v_mul_f32_e32 v140, 0xbf38aa3b, v162
	v_pk_fma_f32 v[164:165], v[160:161], s[22:23], v[90:91] op_sel_hi:[1,0,0]
	v_exp_f32_e32 v162, v140
	v_pk_fma_f32 v[164:165], v[160:161], v[164:165], s[24:25] op_sel_hi:[1,1,0]
	v_mul_f32_e32 v140, 0xbf38aa3b, v163
	v_pk_fma_f32 v[164:165], v[160:161], v[164:165], s[34:35] op_sel_hi:[1,1,0]
	v_and_b32_e32 v159, 0x7fffffff, v157
	v_pk_fma_f32 v[164:165], v[160:161], v[164:165], s[40:41] op_sel_hi:[1,1,0]
	v_and_b32_e32 v158, 0x7fffffff, v156
	v_exp_f32_e32 v163, v140
	v_pk_mul_f32 v[160:161], v[160:161], v[164:165]
	v_fma_f32 v140, |v110|, s25, 1.0
	v_pk_mul_f32 v[158:159], v[158:159], v[160:161]
	v_rcp_f32_e32 v160, v140
	v_fma_f32 v140, |v111|, s25, 1.0
	v_rcp_f32_e32 v161, v140
	v_max_f32_e32 v156, 0, v156
	v_max_f32_e32 v157, 0, v157
	v_pk_fma_f32 v[156:157], v[162:163], v[158:159], v[156:157] neg_lo:[1,0,0] neg_hi:[1,0,0]
	v_pk_mul_f32 v[162:163], v[110:111], v[110:111]
	v_pk_fma_f32 v[164:165], v[160:161], s[22:23], v[90:91] op_sel_hi:[1,0,0]
	v_mul_f32_e32 v140, 0xbf38aa3b, v162
	v_exp_f32_e32 v162, v140
	v_pk_fma_f32 v[164:165], v[160:161], v[164:165], s[24:25] op_sel_hi:[1,1,0]
	v_mul_f32_e32 v140, 0xbf38aa3b, v163
	v_pk_fma_f32 v[164:165], v[160:161], v[164:165], s[34:35] op_sel_hi:[1,1,0]
	v_exp_f32_e32 v163, v140
	v_pk_fma_f32 v[164:165], v[160:161], v[164:165], s[40:41] op_sel_hi:[1,1,0]
	v_and_b32_e32 v159, 0x7fffffff, v111
	v_and_b32_e32 v158, 0x7fffffff, v110
	v_pk_mul_f32 v[160:161], v[160:161], v[164:165]
	v_max_f32_e32 v110, 0, v110
	v_max_f32_e32 v111, 0, v111
	v_pk_mul_f32 v[158:159], v[158:159], v[160:161]
	v_readlane_b32 s0, v154, 2
	v_pk_fma_f32 v[110:111], v[162:163], v[158:159], v[110:111] neg_lo:[1,0,0] neg_hi:[1,0,0]
	v_cvt_pk_f16_f32 v156, v156, v157
	v_pk_mul_f32 v[108:109], s[0:1], v[108:109] op_sel_hi:[0,1]
	v_cvt_pk_f16_f32 v157, v110, v111
	v_pk_fma_f32 v[108:109], v[108:109], v[238:239], v[242:243]
	ds_write_b64 v138, v[156:157] offset:33280
	v_fma_f32 v138, |v108|, s25, 1.0
	v_rcp_f32_e32 v156, v138
	v_fma_f32 v138, |v109|, s25, 1.0
	v_rcp_f32_e32 v157, v138
	v_pk_mul_f32 v[158:159], v[108:109], v[108:109]
	v_and_b32_e32 v111, 0x7fffffff, v109
	v_mul_f32_e32 v138, 0xbf38aa3b, v158
	v_pk_fma_f32 v[160:161], v[156:157], s[22:23], v[90:91] op_sel_hi:[1,0,0]
	v_exp_f32_e32 v158, v138
	v_pk_fma_f32 v[160:161], v[156:157], v[160:161], s[24:25] op_sel_hi:[1,1,0]
	v_mul_f32_e32 v138, 0xbf38aa3b, v159
	v_pk_fma_f32 v[160:161], v[156:157], v[160:161], s[34:35] op_sel_hi:[1,1,0]
	v_exp_f32_e32 v159, v138
	v_pk_fma_f32 v[160:161], v[156:157], v[160:161], s[40:41] op_sel_hi:[1,1,0]
	v_and_b32_e32 v110, 0x7fffffff, v108
	v_pk_mul_f32 v[156:157], v[156:157], v[160:161]
	v_max_f32_e32 v108, 0, v108
	v_max_f32_e32 v109, 0, v109
	v_pk_mul_f32 v[110:111], v[110:111], v[156:157]
	v_pk_mul_f32 v[104:105], s[0:1], v[104:105] op_sel_hi:[0,1]
	v_pk_fma_f32 v[108:109], v[158:159], v[110:111], v[108:109] neg_lo:[1,0,0] neg_hi:[1,0,0]
	v_pk_fma_f32 v[104:105], v[104:105], v[240:241], v[244:245]
	v_cvt_pk_f16_f32 v108, v108, v109
	v_fma_f32 v109, |v104|, s25, 1.0
	v_rcp_f32_e32 v156, v109
	v_fma_f32 v109, |v105|, s25, 1.0
	v_rcp_f32_e32 v157, v109
	v_pk_mul_f32 v[158:159], v[104:105], v[104:105]
	v_and_b32_e32 v111, 0x7fffffff, v105
	v_mul_f32_e32 v109, 0xbf38aa3b, v158
	v_pk_fma_f32 v[160:161], v[156:157], s[22:23], v[90:91] op_sel_hi:[1,0,0]
	v_exp_f32_e32 v158, v109
	v_pk_fma_f32 v[160:161], v[156:157], v[160:161], s[24:25] op_sel_hi:[1,1,0]
	v_mul_f32_e32 v109, 0xbf38aa3b, v159
	v_pk_fma_f32 v[160:161], v[156:157], v[160:161], s[34:35] op_sel_hi:[1,1,0]
	v_exp_f32_e32 v159, v109
	v_pk_fma_f32 v[160:161], v[156:157], v[160:161], s[40:41] op_sel_hi:[1,1,0]
	v_and_b32_e32 v110, 0x7fffffff, v104
	v_pk_mul_f32 v[156:157], v[156:157], v[160:161]
	v_max_f32_e32 v104, 0, v104
	v_max_f32_e32 v105, 0, v105
	v_pk_mul_f32 v[110:111], v[110:111], v[156:157]
	v_readlane_b32 s0, v154, 3
	v_pk_fma_f32 v[104:105], v[158:159], v[110:111], v[104:105] neg_lo:[1,0,0] neg_hi:[1,0,0]
	s_nop 0
	v_pk_mul_f32 v[102:103], s[0:1], v[102:103] op_sel_hi:[0,1]
	v_cvt_pk_f16_f32 v109, v104, v105
	v_pk_fma_f32 v[102:103], v[102:103], v[238:239], v[242:243]
	ds_write_b64 v135, v[108:109] offset:33792
	v_fma_f32 v108, |v102|, s25, 1.0
	v_fma_f32 v109, |v103|, s25, 1.0
	v_rcp_f32_e32 v108, v108
	v_rcp_f32_e32 v109, v109
	v_pk_mul_f32 v[110:111], v[102:103], v[102:103]
	v_and_b32_e32 v105, 0x7fffffff, v103
	v_mul_f32_e32 v110, 0xbf38aa3b, v110
	v_pk_fma_f32 v[156:157], v[108:109], s[22:23], v[90:91] op_sel_hi:[1,0,0]
	v_mul_f32_e32 v111, 0xbf38aa3b, v111
	v_pk_fma_f32 v[156:157], v[108:109], v[156:157], s[24:25] op_sel_hi:[1,1,0]
	v_exp_f32_e32 v110, v110
	v_pk_fma_f32 v[156:157], v[108:109], v[156:157], s[34:35] op_sel_hi:[1,1,0]
	v_exp_f32_e32 v111, v111
	v_pk_fma_f32 v[156:157], v[108:109], v[156:157], s[40:41] op_sel_hi:[1,1,0]
	v_and_b32_e32 v104, 0x7fffffff, v102
	v_pk_mul_f32 v[108:109], v[108:109], v[156:157]
	v_max_f32_e32 v102, 0, v102
	v_max_f32_e32 v103, 0, v103
	v_pk_mul_f32 v[104:105], v[104:105], v[108:109]
	v_pk_mul_f32 v[100:101], s[0:1], v[100:101] op_sel_hi:[0,1]
	v_pk_fma_f32 v[102:103], v[110:111], v[104:105], v[102:103] neg_lo:[1,0,0] neg_hi:[1,0,0]
	v_pk_fma_f32 v[100:101], v[100:101], v[240:241], v[244:245]
	v_cvt_pk_f16_f32 v102, v102, v103
	v_fma_f32 v103, |v100|, s25, 1.0
	v_rcp_f32_e32 v108, v103
	v_fma_f32 v103, |v101|, s25, 1.0
	v_rcp_f32_e32 v109, v103
	v_pk_mul_f32 v[110:111], v[100:101], v[100:101]
	v_and_b32_e32 v105, 0x7fffffff, v101
	v_mul_f32_e32 v103, 0xbf38aa3b, v110
	v_pk_fma_f32 v[156:157], v[108:109], s[22:23], v[90:91] op_sel_hi:[1,0,0]
	v_exp_f32_e32 v110, v103
	v_pk_fma_f32 v[156:157], v[108:109], v[156:157], s[24:25] op_sel_hi:[1,1,0]
	v_mul_f32_e32 v103, 0xbf38aa3b, v111
	v_pk_fma_f32 v[156:157], v[108:109], v[156:157], s[34:35] op_sel_hi:[1,1,0]
	v_exp_f32_e32 v111, v103
	v_pk_fma_f32 v[156:157], v[108:109], v[156:157], s[40:41] op_sel_hi:[1,1,0]
	v_and_b32_e32 v104, 0x7fffffff, v100
	v_pk_mul_f32 v[108:109], v[108:109], v[156:157]
	v_max_f32_e32 v100, 0, v100
	v_max_f32_e32 v101, 0, v101
	v_pk_mul_f32 v[104:105], v[104:105], v[108:109]
	v_readlane_b32 s0, v154, 4
	v_pk_fma_f32 v[100:101], v[110:111], v[104:105], v[100:101] neg_lo:[1,0,0] neg_hi:[1,0,0]
	s_nop 0
	v_pk_mul_f32 v[98:99], s[0:1], v[98:99] op_sel_hi:[0,1]
	v_cvt_pk_f16_f32 v103, v100, v101
	v_pk_fma_f32 v[98:99], v[98:99], v[238:239], v[242:243]
	ds_write_b64 v134, v[102:103] offset:34304
	v_fma_f32 v102, |v98|, s25, 1.0
	v_fma_f32 v103, |v99|, s25, 1.0
	v_rcp_f32_e32 v102, v102
	v_rcp_f32_e32 v103, v103
	v_pk_mul_f32 v[104:105], v[98:99], v[98:99]
	v_and_b32_e32 v101, 0x7fffffff, v99
	v_mul_f32_e32 v104, 0xbf38aa3b, v104
	v_pk_fma_f32 v[108:109], v[102:103], s[22:23], v[90:91] op_sel_hi:[1,0,0]
	v_mul_f32_e32 v105, 0xbf38aa3b, v105
	v_pk_fma_f32 v[108:109], v[102:103], v[108:109], s[24:25] op_sel_hi:[1,1,0]
	v_exp_f32_e32 v104, v104
	v_pk_fma_f32 v[108:109], v[102:103], v[108:109], s[34:35] op_sel_hi:[1,1,0]
	v_exp_f32_e32 v105, v105
	v_pk_fma_f32 v[108:109], v[102:103], v[108:109], s[40:41] op_sel_hi:[1,1,0]
	v_and_b32_e32 v100, 0x7fffffff, v98
	v_pk_mul_f32 v[102:103], v[102:103], v[108:109]
	v_max_f32_e32 v98, 0, v98
	v_max_f32_e32 v99, 0, v99
	v_pk_mul_f32 v[100:101], v[100:101], v[102:103]
	v_pk_mul_f32 v[96:97], s[0:1], v[96:97] op_sel_hi:[0,1]
	v_pk_fma_f32 v[98:99], v[104:105], v[100:101], v[98:99] neg_lo:[1,0,0] neg_hi:[1,0,0]
	v_pk_fma_f32 v[96:97], v[96:97], v[240:241], v[244:245]
	v_cvt_pk_f16_f32 v98, v98, v99
	v_fma_f32 v99, |v96|, s25, 1.0
	v_rcp_f32_e32 v102, v99
	v_fma_f32 v99, |v97|, s25, 1.0
	v_rcp_f32_e32 v103, v99
	v_pk_mul_f32 v[104:105], v[96:97], v[96:97]
	v_and_b32_e32 v101, 0x7fffffff, v97
	v_mul_f32_e32 v99, 0xbf38aa3b, v104
	v_pk_fma_f32 v[108:109], v[102:103], s[22:23], v[90:91] op_sel_hi:[1,0,0]
	v_exp_f32_e32 v104, v99
	v_pk_fma_f32 v[108:109], v[102:103], v[108:109], s[24:25] op_sel_hi:[1,1,0]
	v_mul_f32_e32 v99, 0xbf38aa3b, v105
	v_pk_fma_f32 v[108:109], v[102:103], v[108:109], s[34:35] op_sel_hi:[1,1,0]
	v_exp_f32_e32 v105, v99
	v_pk_fma_f32 v[108:109], v[102:103], v[108:109], s[40:41] op_sel_hi:[1,1,0]
	v_and_b32_e32 v100, 0x7fffffff, v96
	v_pk_mul_f32 v[102:103], v[102:103], v[108:109]
	v_max_f32_e32 v96, 0, v96
	v_max_f32_e32 v97, 0, v97
	v_pk_mul_f32 v[100:101], v[100:101], v[102:103]
	v_readlane_b32 s0, v154, 5
	v_pk_fma_f32 v[96:97], v[104:105], v[100:101], v[96:97] neg_lo:[1,0,0] neg_hi:[1,0,0]
	v_mov_b32_e32 v104, 0
	v_pk_mul_f32 v[94:95], s[0:1], v[94:95] op_sel_hi:[0,1]
	v_cvt_pk_f16_f32 v99, v96, v97
	v_pk_fma_f32 v[94:95], v[94:95], v[238:239], v[242:243]
	ds_write_b64 v120, v[98:99] offset:34816
	v_fma_f32 v98, |v94|, s25, 1.0
	v_fma_f32 v99, |v95|, s25, 1.0
	v_rcp_f32_e32 v98, v98
	v_rcp_f32_e32 v99, v99
	v_pk_mul_f32 v[100:101], v[94:95], v[94:95]
	v_and_b32_e32 v97, 0x7fffffff, v95
	v_mul_f32_e32 v100, 0xbf38aa3b, v100
	v_pk_fma_f32 v[102:103], v[98:99], s[22:23], v[90:91] op_sel_hi:[1,0,0]
	v_mul_f32_e32 v101, 0xbf38aa3b, v101
	v_pk_fma_f32 v[102:103], v[98:99], v[102:103], s[24:25] op_sel_hi:[1,1,0]
	v_exp_f32_e32 v100, v100
	v_pk_fma_f32 v[102:103], v[98:99], v[102:103], s[34:35] op_sel_hi:[1,1,0]
	v_exp_f32_e32 v101, v101
	v_pk_fma_f32 v[102:103], v[98:99], v[102:103], s[40:41] op_sel_hi:[1,1,0]
	v_and_b32_e32 v96, 0x7fffffff, v94
	v_pk_mul_f32 v[98:99], v[98:99], v[102:103]
	v_max_f32_e32 v94, 0, v94
	v_max_f32_e32 v95, 0, v95
	v_pk_mul_f32 v[96:97], v[96:97], v[98:99]
	v_pk_mul_f32 v[92:93], s[0:1], v[92:93] op_sel_hi:[0,1]
	v_pk_fma_f32 v[94:95], v[100:101], v[96:97], v[94:95] neg_lo:[1,0,0] neg_hi:[1,0,0]
	v_pk_fma_f32 v[92:93], v[92:93], v[240:241], v[244:245]
	v_cvt_pk_f16_f32 v94, v94, v95
	v_fma_f32 v95, |v92|, s25, 1.0
	v_rcp_f32_e32 v98, v95
	v_fma_f32 v95, |v93|, s25, 1.0
	v_rcp_f32_e32 v99, v95
	v_pk_mul_f32 v[100:101], v[92:93], v[92:93]
	v_and_b32_e32 v97, 0x7fffffff, v93
	v_mul_f32_e32 v95, 0xbf38aa3b, v100
	v_pk_fma_f32 v[102:103], v[98:99], s[22:23], v[90:91] op_sel_hi:[1,0,0]
	v_exp_f32_e32 v100, v95
	v_pk_fma_f32 v[102:103], v[98:99], v[102:103], s[24:25] op_sel_hi:[1,1,0]
	v_mul_f32_e32 v95, 0xbf38aa3b, v101
	v_pk_fma_f32 v[102:103], v[98:99], v[102:103], s[34:35] op_sel_hi:[1,1,0]
	v_exp_f32_e32 v101, v95
	v_pk_fma_f32 v[102:103], v[98:99], v[102:103], s[40:41] op_sel_hi:[1,1,0]
	v_and_b32_e32 v96, 0x7fffffff, v92
	v_pk_mul_f32 v[98:99], v[98:99], v[102:103]
	v_max_f32_e32 v92, 0, v92
	v_max_f32_e32 v93, 0, v93
	v_pk_mul_f32 v[96:97], v[96:97], v[98:99]
	v_readlane_b32 s0, v154, 6
	v_pk_fma_f32 v[92:93], v[100:101], v[96:97], v[92:93] neg_lo:[1,0,0] neg_hi:[1,0,0]
	s_waitcnt vmcnt(2)
	v_add_f32_e32 v100, v228, v229
	v_pk_mul_f32 v[80:81], s[0:1], v[80:81] op_sel_hi:[0,1]
	v_cvt_pk_f16_f32 v95, v92, v93
	v_pk_fma_f32 v[80:81], v[80:81], v[238:239], v[242:243]
	ds_write_b64 v121, v[94:95] offset:35328
	v_fma_f32 v94, |v80|, s25, 1.0
	v_fma_f32 v95, |v81|, s25, 1.0
	v_rcp_f32_e32 v94, v94
	v_rcp_f32_e32 v95, v95
	v_pk_mul_f32 v[96:97], v[80:81], v[80:81]
	v_and_b32_e32 v93, 0x7fffffff, v81
	v_mul_f32_e32 v96, 0xbf38aa3b, v96
	v_pk_fma_f32 v[98:99], v[94:95], s[22:23], v[90:91] op_sel_hi:[1,0,0]
	v_mul_f32_e32 v97, 0xbf38aa3b, v97
	v_pk_fma_f32 v[98:99], v[94:95], v[98:99], s[24:25] op_sel_hi:[1,1,0]
	v_exp_f32_e32 v96, v96
	v_pk_fma_f32 v[98:99], v[94:95], v[98:99], s[34:35] op_sel_hi:[1,1,0]
	v_exp_f32_e32 v97, v97
	v_pk_fma_f32 v[98:99], v[94:95], v[98:99], s[40:41] op_sel_hi:[1,1,0]
	v_and_b32_e32 v92, 0x7fffffff, v80
	v_pk_mul_f32 v[94:95], v[94:95], v[98:99]
	v_max_f32_e32 v80, 0, v80
	v_max_f32_e32 v81, 0, v81
	v_pk_mul_f32 v[92:93], v[92:93], v[94:95]
	v_pk_mul_f32 v[78:79], s[0:1], v[78:79] op_sel_hi:[0,1]
	v_pk_fma_f32 v[80:81], v[96:97], v[92:93], v[80:81] neg_lo:[1,0,0] neg_hi:[1,0,0]
	v_pk_fma_f32 v[78:79], v[78:79], v[240:241], v[244:245]
	v_cvt_pk_f16_f32 v80, v80, v81
	v_fma_f32 v81, |v78|, s25, 1.0
	v_rcp_f32_e32 v94, v81
	v_fma_f32 v81, |v79|, s25, 1.0
	v_rcp_f32_e32 v95, v81
	v_pk_mul_f32 v[96:97], v[78:79], v[78:79]
	v_and_b32_e32 v93, 0x7fffffff, v79
	v_mul_f32_e32 v81, 0xbf38aa3b, v96
	v_pk_fma_f32 v[98:99], v[94:95], s[22:23], v[90:91] op_sel_hi:[1,0,0]
	v_exp_f32_e32 v96, v81
	v_pk_fma_f32 v[98:99], v[94:95], v[98:99], s[24:25] op_sel_hi:[1,1,0]
	v_mul_f32_e32 v81, 0xbf38aa3b, v97
	v_pk_fma_f32 v[98:99], v[94:95], v[98:99], s[34:35] op_sel_hi:[1,1,0]
	v_exp_f32_e32 v97, v81
	v_pk_fma_f32 v[98:99], v[94:95], v[98:99], s[40:41] op_sel_hi:[1,1,0]
	v_and_b32_e32 v92, 0x7fffffff, v78
	v_pk_mul_f32 v[94:95], v[94:95], v[98:99]
	v_max_f32_e32 v78, 0, v78
	v_max_f32_e32 v79, 0, v79
	v_pk_mul_f32 v[92:93], v[92:93], v[94:95]
	v_readlane_b32 s0, v154, 7
	v_pk_fma_f32 v[78:79], v[96:97], v[92:93], v[78:79] neg_lo:[1,0,0] neg_hi:[1,0,0]
	v_add_f32_e32 v97, v224, v225
	v_pk_mul_f32 v[76:77], s[0:1], v[76:77] op_sel_hi:[0,1]
	v_cvt_pk_f16_f32 v81, v78, v79
	v_pk_fma_f32 v[76:77], v[76:77], v[238:239], v[242:243]
	ds_write_b64 v118, v[80:81] offset:35840
	v_fma_f32 v80, |v76|, s25, 1.0
	v_fma_f32 v81, |v77|, s25, 1.0
	v_rcp_f32_e32 v80, v80
	v_rcp_f32_e32 v81, v81
	v_pk_mul_f32 v[92:93], v[76:77], v[76:77]
	v_and_b32_e32 v79, 0x7fffffff, v77
	v_mul_f32_e32 v92, 0xbf38aa3b, v92
	v_pk_fma_f32 v[94:95], v[80:81], s[22:23], v[90:91] op_sel_hi:[1,0,0]
	v_mul_f32_e32 v93, 0xbf38aa3b, v93
	v_pk_fma_f32 v[94:95], v[80:81], v[94:95], s[24:25] op_sel_hi:[1,1,0]
	v_exp_f32_e32 v92, v92
	v_pk_fma_f32 v[94:95], v[80:81], v[94:95], s[34:35] op_sel_hi:[1,1,0]
	v_exp_f32_e32 v93, v93
	v_pk_fma_f32 v[94:95], v[80:81], v[94:95], s[40:41] op_sel_hi:[1,1,0]
	v_and_b32_e32 v78, 0x7fffffff, v76
	v_pk_mul_f32 v[80:81], v[80:81], v[94:95]
	v_max_f32_e32 v76, 0, v76
	v_max_f32_e32 v77, 0, v77
	v_pk_mul_f32 v[78:79], v[78:79], v[80:81]
	v_pk_mul_f32 v[74:75], s[0:1], v[74:75] op_sel_hi:[0,1]
	v_pk_fma_f32 v[76:77], v[92:93], v[78:79], v[76:77] neg_lo:[1,0,0] neg_hi:[1,0,0]
	v_pk_fma_f32 v[92:93], v[74:75], v[240:241], v[244:245]
	v_cvt_pk_f16_f32 v80, v76, v77
	v_fma_f32 v74, |v92|, s25, 1.0
	v_fma_f32 v75, |v93|, s25, 1.0
	v_rcp_f32_e32 v74, v74
	v_rcp_f32_e32 v75, v75
	v_pk_mul_f32 v[76:77], v[92:93], v[92:93]
	s_waitcnt vmcnt(1)
	v_add_f32_e32 v101, v232, v233
	v_mul_f32_e32 v76, 0xbf38aa3b, v76
	v_pk_fma_f32 v[78:79], v[74:75], s[22:23], v[90:91] op_sel_hi:[1,0,0]
	v_exp_f32_e32 v96, v76
	v_pk_fma_f32 v[78:79], v[74:75], v[78:79], s[24:25] op_sel_hi:[1,1,0]
	v_add_f32_e32 v76, v208, v209
	v_pk_fma_f32 v[78:79], v[74:75], v[78:79], s[34:35] op_sel_hi:[1,1,0]
	v_mul_f32_e32 v81, 0xbf38aa3b, v77
	v_pk_fma_f32 v[78:79], v[74:75], v[78:79], s[40:41] op_sel_hi:[1,1,0]
	v_add_f32_e32 v77, v212, v213
	v_pk_mul_f32 v[98:99], v[74:75], v[78:79]
	v_add_f32_e32 v74, v202, v203
	v_add_f32_e32 v75, v204, v205
	v_add_f32_e32 v74, v74, v75
	v_add_f32_e32 v75, v206, v207
	v_add_f32_e32 v75, v75, v76
	v_add_f32_e32 v76, v210, v211
	v_add_f32_e32 v76, v76, v77
	v_add_f32_e32 v77, v214, v215
	v_add_f32_e32 v78, v216, v217
	v_add_f32_e32 v77, v77, v78
	v_add_f32_e32 v78, v218, v219
	v_add_f32_e32 v79, v220, v221
	v_add_f32_e32 v78, v78, v79
	v_add_f32_e32 v79, v222, v223
	v_add_f32_e32 v79, v79, v97
	v_add_f32_e32 v97, v226, v227
	v_add_f32_e32 v97, v97, v100
	v_add_f32_e32 v100, v230, v231
	v_add_f32_e32 v100, v100, v101
	v_cndmask_b32_e64 v101, v75, v74, s[4:5]
	v_cndmask_b32_e64 v74, v74, v75, s[4:5]
	v_cndmask_b32_e64 v75, v77, v76, s[4:5]
	v_cndmask_b32_e64 v76, v76, v77, s[4:5]
	v_cndmask_b32_e64 v77, v78, v79, s[4:5]
	v_add_f32_dpp v74, v101, v74 quad_perm:[1,0,3,2] row_mask:0xf bank_mask:0xf bound_ctrl:1
	v_add_f32_dpp v75, v75, v76 quad_perm:[1,0,3,2] row_mask:0xf bank_mask:0xf bound_ctrl:1
	v_cndmask_b32_e64 v76, v79, v78, s[4:5]
	v_cndmask_b32_e64 v78, v97, v100, s[4:5]
	v_and_b32_e32 v95, 0x7fffffff, v93
	v_add_f32_dpp v76, v76, v77 quad_perm:[1,0,3,2] row_mask:0xf bank_mask:0xf bound_ctrl:1
	v_cndmask_b32_e64 v77, v100, v97, s[4:5]
	v_exp_f32_e32 v97, v81
	v_and_b32_e32 v94, 0x7fffffff, v92
	v_add_f32_dpp v77, v77, v78 quad_perm:[1,0,3,2] row_mask:0xf bank_mask:0xf bound_ctrl:1
	v_cndmask_b32_e64 v78, v74, v75, s[6:7]
	v_cndmask_b32_e64 v74, v75, v74, s[6:7]
	v_cndmask_b32_e64 v75, v76, v77, s[6:7]
	v_cndmask_b32_e64 v76, v77, v76, s[6:7]
	v_add_f32_dpp v74, v78, v74 quad_perm:[2,3,0,1] row_mask:0xf bank_mask:0xf bound_ctrl:1
	v_max_f32_e32 v92, 0, v92
	v_add_f32_dpp v75, v75, v76 quad_perm:[2,3,0,1] row_mask:0xf bank_mask:0xf bound_ctrl:1
	v_cndmask_b32_e64 v76, v74, v75, s[8:9]
	v_cndmask_b32_e64 v74, v75, v74, s[8:9]
	v_mov_b32_e32 v75, v76
	v_max_f32_e32 v93, 0, v93
	s_waitcnt lgkmcnt(14)
	v_dot2c_f32_f16_e32 v104, v38, v38
	v_mov_b32_dpp v75, v75 row_shl:4 row_mask:0xf bank_mask:0x5
	v_mov_b32_e32 v105, 0
	v_dot2c_f32_f16_e32 v104, v39, v39
	v_mov_b32_dpp v75, v76 row_shr:4 row_mask:0xf bank_mask:0xa
	v_add_f32_e32 v74, v74, v75
	v_dot2c_f32_f16_e32 v104, v40, v40
	v_dot2c_f32_f16_e32 v104, v41, v41
	v_add_f32_dpp v74, v74, v74 row_ror:8 row_mask:0xf bank_mask:0xf bound_ctrl:1
	v_mov_b32_e32 v75, v74
	s_nop 1
	v_permlane16_swap_b32_e32 v74, v75
	v_add_f32_e32 v74, v74, v75
	v_mov_b32_e32 v75, v74
	s_nop 1
	v_permlane32_swap_b32_e32 v74, v75
	v_add_f32_e32 v74, v74, v75
	v_mul_f32_e32 v74, 0x3b800000, v74
	s_waitcnt lgkmcnt(13)
	v_dot2c_f32_f16_e32 v104, v34, v34
	v_readlane_b32 s42, v74, 0
	v_readlane_b32 s44, v74, 1
	v_readlane_b32 s46, v74, 2
	v_pk_add_f32 v[102:103], v[204:205], s[42:43] op_sel_hi:[1, 0] neg_lo:[0, 1] neg_hi:[0, 1]
	v_pk_add_f32 v[78:79], v[208:209], s[44:45] op_sel_hi:[1, 0] neg_lo:[0, 1] neg_hi:[0, 1]
	v_pk_add_f32 v[100:101], v[202:203], s[42:43] op_sel_hi:[1, 0] neg_lo:[0, 1] neg_hi:[0, 1]
	v_mul_f32_e32 v70, v103, v103
	v_mul_f32_e32 v71, v79, v79
	v_fmac_f32_e32 v70, v102, v102
	v_pk_add_f32 v[86:87], v[206:207], s[44:45] op_sel_hi:[1, 0] neg_lo:[0, 1] neg_hi:[0, 1]
	v_fmac_f32_e32 v71, v78, v78
	v_fmac_f32_e32 v70, v101, v101
	v_fmac_f32_e32 v71, v87, v87
	v_fmac_f32_e32 v70, v100, v100
	v_fmac_f32_e32 v71, v86, v86
	v_readlane_b32 s48, v74, 3
	v_cndmask_b32_e64 v72, v71, v70, s[4:5]
	v_cndmask_b32_e64 v70, v70, v71, s[4:5]
	v_readlane_b32 s50, v74, 4
	v_readlane_b32 s52, v74, 5
	v_readlane_b32 s54, v74, 6
	v_readlane_b32 s0, v74, 7
	v_add_f32_dpp v88, v72, v70 quad_perm:[1,0,3,2] row_mask:0xf bank_mask:0xf bound_ctrl:1
	v_pk_add_f32 v[74:75], v[212:213], s[46:47] op_sel_hi:[1, 0] neg_lo:[0, 1] neg_hi:[0, 1]
	v_pk_add_f32 v[70:71], v[216:217], s[48:49] op_sel_hi:[1, 0] neg_lo:[0, 1] neg_hi:[0, 1]
	v_pk_add_f32 v[76:77], v[210:211], s[46:47] op_sel_hi:[1, 0] neg_lo:[0, 1] neg_hi:[0, 1]
	v_mul_f32_e32 v82, v75, v75
	v_pk_add_f32 v[72:73], v[214:215], s[48:49] op_sel_hi:[1, 0] neg_lo:[0, 1] neg_hi:[0, 1]
	v_mul_f32_e32 v66, v71, v71
	v_fmac_f32_e32 v82, v74, v74
	v_fmac_f32_e32 v66, v70, v70
	v_fmac_f32_e32 v82, v77, v77
	v_fmac_f32_e32 v66, v73, v73
	v_fmac_f32_e32 v82, v76, v76
	v_fmac_f32_e32 v66, v72, v72
	v_cndmask_b32_e64 v67, v66, v82, s[4:5]
	v_cndmask_b32_e64 v66, v82, v66, s[4:5]
	v_pk_add_f32 v[68:69], v[218:219], s[50:51] op_sel_hi:[1, 0] neg_lo:[0, 1] neg_hi:[0, 1]
	v_pk_add_f32 v[62:63], v[222:223], s[52:53] op_sel_hi:[1, 0] neg_lo:[0, 1] neg_hi:[0, 1]
	v_add_f32_dpp v66, v67, v66 quad_perm:[1,0,3,2] row_mask:0xf bank_mask:0xf bound_ctrl:1
	v_cndmask_b32_e64 v67, v88, v66, s[6:7]
	v_cndmask_b32_e64 v66, v66, v88, s[6:7]
	v_pk_add_f32 v[56:57], v[228:229], s[54:55] op_sel_hi:[1, 0] neg_lo:[0, 1] neg_hi:[0, 1]
	v_dot2c_f32_f16_e32 v104, v35, v35
	v_add_f32_dpp v82, v67, v66 quad_perm:[2,3,0,1] row_mask:0xf bank_mask:0xf bound_ctrl:1
	v_pk_add_f32 v[66:67], v[220:221], s[50:51] op_sel_hi:[1, 0] neg_lo:[0, 1] neg_hi:[0, 1]
	v_pk_add_f32 v[60:61], v[224:225], s[52:53] op_sel_hi:[1, 0] neg_lo:[0, 1] neg_hi:[0, 1]
	v_mul_f32_e32 v58, v67, v67
	v_mul_f32_e32 v59, v61, v61
	v_fmac_f32_e32 v58, v66, v66
	v_fmac_f32_e32 v59, v60, v60
	v_fmac_f32_e32 v58, v69, v69
	v_fmac_f32_e32 v59, v63, v63
	v_fmac_f32_e32 v58, v68, v68
	v_fmac_f32_e32 v59, v62, v62
	v_cndmask_b32_e64 v64, v59, v58, s[4:5]
	v_cndmask_b32_e64 v58, v58, v59, s[4:5]
	v_mul_f32_e32 v65, v57, v57
	v_fmac_f32_e32 v65, v56, v56
	v_add_f32_dpp v64, v64, v58 quad_perm:[1,0,3,2] row_mask:0xf bank_mask:0xf bound_ctrl:1
	v_pk_add_f32 v[58:59], v[226:227], s[54:55] op_sel_hi:[1, 0] neg_lo:[0, 1] neg_hi:[0, 1]
	v_pk_add_f32 v[54:55], v[230:231], s[0:1] op_sel_hi:[1, 0] neg_lo:[0, 1] neg_hi:[0, 1]
	v_pk_add_f32 v[50:51], v[232:233], s[0:1] op_sel_hi:[1, 0] neg_lo:[0, 1] neg_hi:[0, 1]
	v_fmac_f32_e32 v65, v59, v59
	v_mul_f32_e32 v52, v51, v51
	v_fmac_f32_e32 v52, v50, v50
	v_fmac_f32_e32 v52, v55, v55
	v_fmac_f32_e32 v65, v58, v58
	v_fmac_f32_e32 v52, v54, v54
	v_cndmask_b32_e64 v53, v52, v65, s[4:5]
	v_cndmask_b32_e64 v52, v65, v52, s[4:5]
	v_dot2c_f32_f16_e32 v104, v36, v36
	v_dot2c_f32_f16_e32 v104, v37, v37
	v_add_f32_dpp v52, v53, v52 quad_perm:[1,0,3,2] row_mask:0xf bank_mask:0xf bound_ctrl:1
	v_cndmask_b32_e64 v53, v64, v52, s[6:7]
	v_cndmask_b32_e64 v52, v52, v64, s[6:7]
	s_waitcnt lgkmcnt(12)
	v_dot2c_f32_f16_e32 v104, v30, v30
	v_dot2c_f32_f16_e32 v104, v31, v31
	v_add_f32_dpp v52, v53, v52 quad_perm:[2,3,0,1] row_mask:0xf bank_mask:0xf bound_ctrl:1
	v_cndmask_b32_e64 v53, v82, v52, s[8:9]
	v_mov_b32_e32 v64, v53
	v_cndmask_b32_e64 v52, v52, v82, s[8:9]
	v_dot2c_f32_f16_e32 v104, v32, v32
	v_mov_b32_dpp v64, v64 row_shl:4 row_mask:0xf bank_mask:0x5
	v_dot2c_f32_f16_e32 v104, v33, v33
	s_waitcnt lgkmcnt(11)
	v_dot2c_f32_f16_e32 v104, v26, v26
	v_mov_b32_dpp v64, v53 row_shr:4 row_mask:0xf bank_mask:0xa
	v_add_f32_e32 v52, v52, v64
	v_dot2c_f32_f16_e32 v104, v27, v27
	v_dot2c_f32_f16_e32 v104, v28, v28
	v_add_f32_dpp v52, v52, v52 row_ror:8 row_mask:0xf bank_mask:0xf bound_ctrl:1
	v_mov_b32_e32 v53, v52
	s_nop 1
	v_permlane16_swap_b32_e32 v52, v53
	v_add_f32_e32 v52, v52, v53
	v_mov_b32_e32 v53, v52
	s_nop 1
	v_permlane32_swap_b32_e32 v52, v53
	v_add_f32_e32 v52, v52, v53
	v_fmac_f32_e32 v116, 0x3b800000, v52
	v_mul_f32_e32 v52, 0x4f800000, v116
	v_cmp_gt_f32_e32 vcc, s35, v116
	v_dot2c_f32_f16_e32 v104, v29, v29
	s_waitcnt lgkmcnt(10)
	v_dot2c_f32_f16_e32 v104, v22, v22
	v_cndmask_b32_e32 v64, v116, v52, vcc
	v_sqrt_f32_e32 v65, v64
	v_pk_mul_f32 v[52:53], v[94:95], v[98:99]
	v_and_b32_e32 v94, 48, v0
	v_pk_fma_f32 v[52:53], v[96:97], v[52:53], v[92:93] neg_lo:[1,0,0] neg_hi:[1,0,0]
	v_add_u32_e32 v81, -1, v65
	v_fma_f32 v82, -v81, v65, v64
	v_cmp_ge_f32_e64 s[0:1], 0, v82
	v_add_u32_e32 v82, 1, v65
	v_add_u32_e32 v95, 0x19860, v94
	v_cndmask_b32_e64 v81, v65, v81, s[0:1]
	v_fma_f32 v65, -v82, v65, v64
	v_cmp_lt_f32_e64 s[0:1], 0, v65
	v_dot2c_f32_f16_e32 v104, v23, v23
	v_dot2c_f32_f16_e32 v104, v24, v24
	v_cndmask_b32_e64 v65, v81, v82, s[0:1]
	v_mul_f32_e32 v81, 0x37800000, v65
	v_cndmask_b32_e32 v65, v65, v81, vcc
	v_cmp_class_f32_e32 vcc, v64, v117
	v_cvt_pk_f16_f32 v81, v52, v53
	ds_write_b64 v144, v[80:81] offset:36352
	v_cndmask_b32_e32 v64, v65, v64, vcc
	v_div_scale_f32 v65, s[0:1], v64, v64, 1.0
	v_rcp_f32_e32 v82, v65
	v_dot2c_f32_f16_e32 v104, v25, v25
	s_waitcnt lgkmcnt(10)
	v_dot2c_f32_f16_e32 v104, v18, v18
	v_dot2c_f32_f16_e32 v104, v19, v19
	v_fma_f32 v52, -v65, v82, 1.0
	v_fmac_f32_e32 v82, v52, v82
	v_div_scale_f32 v52, vcc, 1.0, v64, 1.0
	v_mul_f32_e32 v53, v52, v82
	v_fma_f32 v80, -v65, v53, v52
	v_fmac_f32_e32 v53, v80, v82
	v_fma_f32 v52, -v65, v53, v52
	v_div_fmas_f32 v52, v52, v82, v53
	v_div_fixup_f32 v52, v52, v64, 1.0
	v_dot2c_f32_f16_e32 v104, v20, v20
	v_readlane_b32 s0, v52, 0
	v_dot2c_f32_f16_e32 v104, v21, v21
	s_waitcnt lgkmcnt(9)
	v_dot2c_f32_f16_e32 v104, v14, v14
	v_pk_mul_f32 v[64:65], s[0:1], v[100:101] op_sel_hi:[0,1]
	v_pk_fma_f32 v[64:65], v[64:65], v[238:239], v[242:243]
	v_dot2c_f32_f16_e32 v104, v15, v15
	v_fma_f32 v53, |v64|, s25, 1.0
	v_rcp_f32_e32 v82, v53
	v_fma_f32 v53, |v65|, s25, 1.0
	v_rcp_f32_e32 v83, v53
	v_pk_mul_f32 v[84:85], v[64:65], v[64:65]
	v_and_b32_e32 v81, 0x7fffffff, v65
	v_mul_f32_e32 v53, 0xbf38aa3b, v84
	v_pk_fma_f32 v[88:89], v[82:83], s[22:23], v[90:91] op_sel_hi:[1,0,0]
	v_exp_f32_e32 v84, v53
	v_pk_fma_f32 v[88:89], v[82:83], v[88:89], s[24:25] op_sel_hi:[1,1,0]
	v_mul_f32_e32 v53, 0xbf38aa3b, v85
	v_pk_fma_f32 v[88:89], v[82:83], v[88:89], s[34:35] op_sel_hi:[1,1,0]
	v_exp_f32_e32 v85, v53
	v_pk_fma_f32 v[88:89], v[82:83], v[88:89], s[40:41] op_sel_hi:[1,1,0]
	v_and_b32_e32 v80, 0x7fffffff, v64
	v_pk_mul_f32 v[82:83], v[82:83], v[88:89]
	v_max_f32_e32 v64, 0, v64
	v_max_f32_e32 v65, 0, v65
	v_pk_mul_f32 v[80:81], v[80:81], v[82:83]
	v_dot2c_f32_f16_e32 v104, v16, v16
	v_pk_fma_f32 v[64:65], v[84:85], v[80:81], v[64:65] neg_lo:[1,0,0] neg_hi:[1,0,0]
	v_pk_mul_f32 v[80:81], s[0:1], v[102:103] op_sel_hi:[0,1]
	v_pk_fma_f32 v[80:81], v[80:81], v[240:241], v[244:245]
	v_cvt_pk_f16_f32 v64, v64, v65
	v_fma_f32 v53, |v80|, s25, 1.0
	v_rcp_f32_e32 v84, v53
	v_fma_f32 v53, |v81|, s25, 1.0
	v_rcp_f32_e32 v85, v53
	v_pk_mul_f32 v[88:89], v[80:81], v[80:81]
	v_and_b32_e32 v83, 0x7fffffff, v81
	v_mul_f32_e32 v53, 0xbf38aa3b, v88
	v_pk_fma_f32 v[92:93], v[84:85], s[22:23], v[90:91] op_sel_hi:[1,0,0]
	v_exp_f32_e32 v88, v53
	v_pk_fma_f32 v[92:93], v[84:85], v[92:93], s[24:25] op_sel_hi:[1,1,0]
	v_mul_f32_e32 v53, 0xbf38aa3b, v89
	v_pk_fma_f32 v[92:93], v[84:85], v[92:93], s[34:35] op_sel_hi:[1,1,0]
	v_exp_f32_e32 v89, v53
	v_pk_fma_f32 v[92:93], v[84:85], v[92:93], s[40:41] op_sel_hi:[1,1,0]
	v_and_b32_e32 v82, 0x7fffffff, v80
	v_pk_mul_f32 v[84:85], v[84:85], v[92:93]
	v_max_f32_e32 v80, 0, v80
	v_max_f32_e32 v81, 0, v81
	v_pk_mul_f32 v[82:83], v[82:83], v[84:85]
	v_readlane_b32 s0, v52, 1
	v_pk_fma_f32 v[80:81], v[88:89], v[82:83], v[80:81] neg_lo:[1,0,0] neg_hi:[1,0,0]
	v_dot2c_f32_f16_e32 v104, v17, v17
	v_cvt_pk_f16_f32 v65, v80, v81
	ds_write_b64 v145, v[64:65] offset:36864
	v_pk_mul_f32 v[64:65], s[0:1], v[86:87] op_sel_hi:[0,1]
	v_pk_fma_f32 v[64:65], v[64:65], v[238:239], v[242:243]
	v_pk_mul_f32 v[78:79], s[0:1], v[78:79] op_sel_hi:[0,1]
	v_fma_f32 v53, |v64|, s25, 1.0
	v_rcp_f32_e32 v82, v53
	v_fma_f32 v53, |v65|, s25, 1.0
	v_rcp_f32_e32 v83, v53
	v_pk_mul_f32 v[84:85], v[64:65], v[64:65]
	v_pk_fma_f32 v[78:79], v[78:79], v[240:241], v[244:245]
	v_mul_f32_e32 v53, 0xbf38aa3b, v84
	v_pk_fma_f32 v[86:87], v[82:83], s[22:23], v[90:91] op_sel_hi:[1,0,0]
	v_exp_f32_e32 v84, v53
	v_pk_fma_f32 v[86:87], v[82:83], v[86:87], s[24:25] op_sel_hi:[1,1,0]
	v_mul_f32_e32 v53, 0xbf38aa3b, v85
	v_pk_fma_f32 v[86:87], v[82:83], v[86:87], s[34:35] op_sel_hi:[1,1,0]
	v_and_b32_e32 v81, 0x7fffffff, v65
	v_pk_fma_f32 v[86:87], v[82:83], v[86:87], s[40:41] op_sel_hi:[1,1,0]
	v_and_b32_e32 v80, 0x7fffffff, v64
	v_exp_f32_e32 v85, v53
	v_pk_mul_f32 v[82:83], v[82:83], v[86:87]
	v_fma_f32 v53, |v78|, s25, 1.0
	v_pk_mul_f32 v[80:81], v[80:81], v[82:83]
	v_rcp_f32_e32 v82, v53
	v_fma_f32 v53, |v79|, s25, 1.0
	v_rcp_f32_e32 v83, v53
	v_max_f32_e32 v64, 0, v64
	v_max_f32_e32 v65, 0, v65
	v_pk_fma_f32 v[64:65], v[84:85], v[80:81], v[64:65] neg_lo:[1,0,0] neg_hi:[1,0,0]
	v_pk_mul_f32 v[84:85], v[78:79], v[78:79]
	v_pk_fma_f32 v[86:87], v[82:83], s[22:23], v[90:91] op_sel_hi:[1,0,0]
	v_mul_f32_e32 v53, 0xbf38aa3b, v84
	v_exp_f32_e32 v84, v53
	v_pk_fma_f32 v[86:87], v[82:83], v[86:87], s[24:25] op_sel_hi:[1,1,0]
	v_mul_f32_e32 v53, 0xbf38aa3b, v85
	v_pk_fma_f32 v[86:87], v[82:83], v[86:87], s[34:35] op_sel_hi:[1,1,0]
	v_exp_f32_e32 v85, v53
	v_pk_fma_f32 v[86:87], v[82:83], v[86:87], s[40:41] op_sel_hi:[1,1,0]
	v_and_b32_e32 v81, 0x7fffffff, v79
	v_and_b32_e32 v80, 0x7fffffff, v78
	v_pk_mul_f32 v[82:83], v[82:83], v[86:87]
	v_max_f32_e32 v78, 0, v78
	v_max_f32_e32 v79, 0, v79
	v_pk_mul_f32 v[80:81], v[80:81], v[82:83]
	v_cvt_pk_f16_f32 v64, v64, v65
	v_pk_fma_f32 v[78:79], v[84:85], v[80:81], v[78:79] neg_lo:[1,0,0] neg_hi:[1,0,0]
	v_readlane_b32 s0, v52, 2
	v_cvt_pk_f16_f32 v65, v78, v79
	ds_write_b64 v139, v[64:65] offset:37376
	v_pk_mul_f32 v[64:65], s[0:1], v[76:77] op_sel_hi:[0,1]
	v_pk_fma_f32 v[64:65], v[64:65], v[238:239], v[242:243]
	v_pk_mul_f32 v[74:75], s[0:1], v[74:75] op_sel_hi:[0,1]
	v_fma_f32 v53, |v64|, s25, 1.0
	v_rcp_f32_e32 v78, v53
	v_fma_f32 v53, |v65|, s25, 1.0
	v_rcp_f32_e32 v79, v53
	v_pk_mul_f32 v[80:81], v[64:65], v[64:65]
	v_pk_fma_f32 v[74:75], v[74:75], v[240:241], v[244:245]
	v_mul_f32_e32 v53, 0xbf38aa3b, v80
	v_pk_fma_f32 v[82:83], v[78:79], s[22:23], v[90:91] op_sel_hi:[1,0,0]
	v_exp_f32_e32 v80, v53
	v_pk_fma_f32 v[82:83], v[78:79], v[82:83], s[24:25] op_sel_hi:[1,1,0]
	v_mul_f32_e32 v53, 0xbf38aa3b, v81
	v_pk_fma_f32 v[82:83], v[78:79], v[82:83], s[34:35] op_sel_hi:[1,1,0]
	v_and_b32_e32 v77, 0x7fffffff, v65
	v_pk_fma_f32 v[82:83], v[78:79], v[82:83], s[40:41] op_sel_hi:[1,1,0]
	v_and_b32_e32 v76, 0x7fffffff, v64
	v_exp_f32_e32 v81, v53
	v_pk_mul_f32 v[78:79], v[78:79], v[82:83]
	v_fma_f32 v53, |v74|, s25, 1.0
	v_pk_mul_f32 v[76:77], v[76:77], v[78:79]
	v_rcp_f32_e32 v78, v53
	v_fma_f32 v53, |v75|, s25, 1.0
	v_rcp_f32_e32 v79, v53
	v_max_f32_e32 v64, 0, v64
	v_max_f32_e32 v65, 0, v65
	v_pk_fma_f32 v[64:65], v[80:81], v[76:77], v[64:65] neg_lo:[1,0,0] neg_hi:[1,0,0]
	v_pk_mul_f32 v[80:81], v[74:75], v[74:75]
	v_pk_fma_f32 v[82:83], v[78:79], s[22:23], v[90:91] op_sel_hi:[1,0,0]
	v_mul_f32_e32 v53, 0xbf38aa3b, v80
	v_exp_f32_e32 v80, v53
	v_pk_fma_f32 v[82:83], v[78:79], v[82:83], s[24:25] op_sel_hi:[1,1,0]
	v_mul_f32_e32 v53, 0xbf38aa3b, v81
	v_pk_fma_f32 v[82:83], v[78:79], v[82:83], s[34:35] op_sel_hi:[1,1,0]
	v_exp_f32_e32 v81, v53
	v_pk_fma_f32 v[82:83], v[78:79], v[82:83], s[40:41] op_sel_hi:[1,1,0]
	v_and_b32_e32 v77, 0x7fffffff, v75
	v_and_b32_e32 v76, 0x7fffffff, v74
	v_pk_mul_f32 v[78:79], v[78:79], v[82:83]
	v_max_f32_e32 v74, 0, v74
	v_max_f32_e32 v75, 0, v75
	v_pk_mul_f32 v[76:77], v[76:77], v[78:79]
	v_cvt_pk_f16_f32 v64, v64, v65
	v_pk_fma_f32 v[74:75], v[80:81], v[76:77], v[74:75] neg_lo:[1,0,0] neg_hi:[1,0,0]
	v_readlane_b32 s0, v52, 3
	v_cvt_pk_f16_f32 v65, v74, v75
	ds_write_b64 v137, v[64:65] offset:37888
	v_pk_mul_f32 v[64:65], s[0:1], v[72:73] op_sel_hi:[0,1]
	v_pk_fma_f32 v[64:65], v[64:65], v[238:239], v[242:243]
	v_pk_mul_f32 v[70:71], s[0:1], v[70:71] op_sel_hi:[0,1]
	v_fma_f32 v53, |v64|, s25, 1.0
	v_rcp_f32_e32 v74, v53
	v_fma_f32 v53, |v65|, s25, 1.0
	v_rcp_f32_e32 v75, v53
	v_pk_mul_f32 v[76:77], v[64:65], v[64:65]
	v_pk_fma_f32 v[70:71], v[70:71], v[240:241], v[244:245]
	v_mul_f32_e32 v53, 0xbf38aa3b, v76
	v_pk_fma_f32 v[78:79], v[74:75], s[22:23], v[90:91] op_sel_hi:[1,0,0]
	v_exp_f32_e32 v76, v53
	v_pk_fma_f32 v[78:79], v[74:75], v[78:79], s[24:25] op_sel_hi:[1,1,0]
	v_mul_f32_e32 v53, 0xbf38aa3b, v77
	v_pk_fma_f32 v[78:79], v[74:75], v[78:79], s[34:35] op_sel_hi:[1,1,0]
	v_and_b32_e32 v73, 0x7fffffff, v65
	v_pk_fma_f32 v[78:79], v[74:75], v[78:79], s[40:41] op_sel_hi:[1,1,0]
	v_and_b32_e32 v72, 0x7fffffff, v64
	v_exp_f32_e32 v77, v53
	v_pk_mul_f32 v[74:75], v[74:75], v[78:79]
	v_fma_f32 v53, |v70|, s25, 1.0
	v_pk_mul_f32 v[72:73], v[72:73], v[74:75]
	v_rcp_f32_e32 v74, v53
	v_fma_f32 v53, |v71|, s25, 1.0
	v_rcp_f32_e32 v75, v53
	v_max_f32_e32 v64, 0, v64
	v_max_f32_e32 v65, 0, v65
	v_pk_fma_f32 v[64:65], v[76:77], v[72:73], v[64:65] neg_lo:[1,0,0] neg_hi:[1,0,0]
	v_pk_mul_f32 v[76:77], v[70:71], v[70:71]
	v_pk_fma_f32 v[78:79], v[74:75], s[22:23], v[90:91] op_sel_hi:[1,0,0]
	v_mul_f32_e32 v53, 0xbf38aa3b, v76
	v_exp_f32_e32 v76, v53
	v_pk_fma_f32 v[78:79], v[74:75], v[78:79], s[24:25] op_sel_hi:[1,1,0]
	v_mul_f32_e32 v53, 0xbf38aa3b, v77
	v_pk_fma_f32 v[78:79], v[74:75], v[78:79], s[34:35] op_sel_hi:[1,1,0]
	v_exp_f32_e32 v77, v53
	v_pk_fma_f32 v[78:79], v[74:75], v[78:79], s[40:41] op_sel_hi:[1,1,0]
	v_and_b32_e32 v73, 0x7fffffff, v71
	v_and_b32_e32 v72, 0x7fffffff, v70
	v_pk_mul_f32 v[74:75], v[74:75], v[78:79]
	v_max_f32_e32 v70, 0, v70
	v_max_f32_e32 v71, 0, v71
	v_pk_mul_f32 v[72:73], v[72:73], v[74:75]
	v_cvt_pk_f16_f32 v64, v64, v65
	v_pk_fma_f32 v[70:71], v[76:77], v[72:73], v[70:71] neg_lo:[1,0,0] neg_hi:[1,0,0]
	v_readlane_b32 s0, v52, 4
	v_cvt_pk_f16_f32 v65, v70, v71
	ds_write_b64 v136, v[64:65] offset:38400
	v_pk_mul_f32 v[64:65], s[0:1], v[68:69] op_sel_hi:[0,1]
	v_pk_fma_f32 v[64:65], v[64:65], v[238:239], v[242:243]
	v_pk_mul_f32 v[66:67], s[0:1], v[66:67] op_sel_hi:[0,1]
	v_fma_f32 v53, |v64|, s25, 1.0
	v_rcp_f32_e32 v70, v53
	v_fma_f32 v53, |v65|, s25, 1.0
	v_rcp_f32_e32 v71, v53
	v_pk_mul_f32 v[72:73], v[64:65], v[64:65]
	v_pk_fma_f32 v[66:67], v[66:67], v[240:241], v[244:245]
	v_mul_f32_e32 v53, 0xbf38aa3b, v72
	v_pk_fma_f32 v[74:75], v[70:71], s[22:23], v[90:91] op_sel_hi:[1,0,0]
	v_exp_f32_e32 v72, v53
	v_pk_fma_f32 v[74:75], v[70:71], v[74:75], s[24:25] op_sel_hi:[1,1,0]
	v_mul_f32_e32 v53, 0xbf38aa3b, v73
	v_pk_fma_f32 v[74:75], v[70:71], v[74:75], s[34:35] op_sel_hi:[1,1,0]
	v_and_b32_e32 v69, 0x7fffffff, v65
	v_pk_fma_f32 v[74:75], v[70:71], v[74:75], s[40:41] op_sel_hi:[1,1,0]
	v_and_b32_e32 v68, 0x7fffffff, v64
	v_exp_f32_e32 v73, v53
	v_pk_mul_f32 v[70:71], v[70:71], v[74:75]
	v_fma_f32 v53, |v66|, s25, 1.0
	v_pk_mul_f32 v[68:69], v[68:69], v[70:71]
	v_rcp_f32_e32 v70, v53
	v_fma_f32 v53, |v67|, s25, 1.0
	v_rcp_f32_e32 v71, v53
	v_max_f32_e32 v64, 0, v64
	v_max_f32_e32 v65, 0, v65
	v_pk_fma_f32 v[64:65], v[72:73], v[68:69], v[64:65] neg_lo:[1,0,0] neg_hi:[1,0,0]
	v_pk_mul_f32 v[72:73], v[66:67], v[66:67]
	v_pk_fma_f32 v[74:75], v[70:71], s[22:23], v[90:91] op_sel_hi:[1,0,0]
	v_mul_f32_e32 v53, 0xbf38aa3b, v72
	v_exp_f32_e32 v72, v53
	v_pk_fma_f32 v[74:75], v[70:71], v[74:75], s[24:25] op_sel_hi:[1,1,0]
	v_mul_f32_e32 v53, 0xbf38aa3b, v73
	v_pk_fma_f32 v[74:75], v[70:71], v[74:75], s[34:35] op_sel_hi:[1,1,0]
	v_exp_f32_e32 v73, v53
	v_pk_fma_f32 v[74:75], v[70:71], v[74:75], s[40:41] op_sel_hi:[1,1,0]
	v_readlane_b32 s0, v52, 5
	v_and_b32_e32 v69, 0x7fffffff, v67
	v_and_b32_e32 v68, 0x7fffffff, v66
	v_pk_mul_f32 v[70:71], v[70:71], v[74:75]
	v_pk_mul_f32 v[62:63], s[0:1], v[62:63] op_sel_hi:[0,1]
	v_max_f32_e32 v66, 0, v66
	v_max_f32_e32 v67, 0, v67
	v_pk_mul_f32 v[68:69], v[68:69], v[70:71]
	v_pk_fma_f32 v[62:63], v[62:63], v[238:239], v[242:243]
	v_pk_fma_f32 v[66:67], v[72:73], v[68:69], v[66:67] neg_lo:[1,0,0] neg_hi:[1,0,0]
	v_fma_f32 v53, |v62|, s25, 1.0
	v_cvt_pk_f16_f32 v64, v64, v65
	v_cvt_pk_f16_f32 v65, v66, v67
	v_rcp_f32_e32 v66, v53
	v_fma_f32 v53, |v63|, s25, 1.0
	v_rcp_f32_e32 v67, v53
	v_pk_mul_f32 v[68:69], v[62:63], v[62:63]
	v_pk_mul_f32 v[60:61], s[0:1], v[60:61] op_sel_hi:[0,1]
	v_mul_f32_e32 v53, 0xbf38aa3b, v68
	v_pk_fma_f32 v[70:71], v[66:67], s[22:23], v[90:91] op_sel_hi:[1,0,0]
	v_exp_f32_e32 v68, v53
	v_pk_fma_f32 v[70:71], v[66:67], v[70:71], s[24:25] op_sel_hi:[1,1,0]
	v_mul_f32_e32 v53, 0xbf38aa3b, v69
	v_pk_fma_f32 v[70:71], v[66:67], v[70:71], s[34:35] op_sel_hi:[1,1,0]
	v_pk_fma_f32 v[60:61], v[60:61], v[240:241], v[244:245]
	v_pk_fma_f32 v[70:71], v[66:67], v[70:71], s[40:41] op_sel_hi:[1,1,0]
	ds_write_b64 v123, v[64:65] offset:38912
	v_and_b32_e32 v65, 0x7fffffff, v63
	v_and_b32_e32 v64, 0x7fffffff, v62
	v_exp_f32_e32 v69, v53
	v_pk_mul_f32 v[66:67], v[66:67], v[70:71]
	v_fma_f32 v53, |v60|, s25, 1.0
	v_pk_mul_f32 v[64:65], v[64:65], v[66:67]
	v_rcp_f32_e32 v66, v53
	v_fma_f32 v53, |v61|, s25, 1.0
	v_rcp_f32_e32 v67, v53
	v_max_f32_e32 v62, 0, v62
	v_max_f32_e32 v63, 0, v63
	v_pk_fma_f32 v[62:63], v[68:69], v[64:65], v[62:63] neg_lo:[1,0,0] neg_hi:[1,0,0]
	v_pk_mul_f32 v[68:69], v[60:61], v[60:61]
	v_pk_fma_f32 v[70:71], v[66:67], s[22:23], v[90:91] op_sel_hi:[1,0,0]
	v_mul_f32_e32 v53, 0xbf38aa3b, v68
	v_exp_f32_e32 v68, v53
	v_pk_fma_f32 v[70:71], v[66:67], v[70:71], s[24:25] op_sel_hi:[1,1,0]
	v_mul_f32_e32 v53, 0xbf38aa3b, v69
	v_pk_fma_f32 v[70:71], v[66:67], v[70:71], s[34:35] op_sel_hi:[1,1,0]
	v_exp_f32_e32 v69, v53
	v_pk_fma_f32 v[70:71], v[66:67], v[70:71], s[40:41] op_sel_hi:[1,1,0]
	v_and_b32_e32 v65, 0x7fffffff, v61
	v_and_b32_e32 v64, 0x7fffffff, v60
	v_pk_mul_f32 v[66:67], v[66:67], v[70:71]
	v_readlane_b32 s0, v52, 6
	v_max_f32_e32 v60, 0, v60
	v_max_f32_e32 v61, 0, v61
	v_pk_mul_f32 v[64:65], v[64:65], v[66:67]
	v_pk_mul_f32 v[58:59], s[0:1], v[58:59] op_sel_hi:[0,1]
	v_pk_fma_f32 v[60:61], v[68:69], v[64:65], v[60:61] neg_lo:[1,0,0] neg_hi:[1,0,0]
	v_pk_fma_f32 v[58:59], v[58:59], v[238:239], v[242:243]
	v_cvt_pk_f16_f32 v62, v62, v63
	v_cvt_pk_f16_f32 v63, v60, v61
	v_fma_f32 v53, |v58|, s25, 1.0
	ds_write_b64 v133, v[62:63] offset:39424
	v_rcp_f32_e32 v62, v53
	v_fma_f32 v53, |v59|, s25, 1.0
	v_rcp_f32_e32 v63, v53
	v_pk_mul_f32 v[64:65], v[58:59], v[58:59]
	v_pk_mul_f32 v[56:57], s[0:1], v[56:57] op_sel_hi:[0,1]
	v_mul_f32_e32 v53, 0xbf38aa3b, v64
	v_pk_fma_f32 v[66:67], v[62:63], s[22:23], v[90:91] op_sel_hi:[1,0,0]
	v_exp_f32_e32 v64, v53
	v_pk_fma_f32 v[66:67], v[62:63], v[66:67], s[24:25] op_sel_hi:[1,1,0]
	v_mul_f32_e32 v53, 0xbf38aa3b, v65
	v_pk_fma_f32 v[66:67], v[62:63], v[66:67], s[34:35] op_sel_hi:[1,1,0]
	v_exp_f32_e32 v65, v53
	v_pk_fma_f32 v[66:67], v[62:63], v[66:67], s[40:41] op_sel_hi:[1,1,0]
	v_pk_fma_f32 v[56:57], v[56:57], v[240:241], v[244:245]
	v_and_b32_e32 v61, 0x7fffffff, v59
	v_and_b32_e32 v60, 0x7fffffff, v58
	v_pk_mul_f32 v[62:63], v[62:63], v[66:67]
	v_fma_f32 v53, |v56|, s25, 1.0
	v_pk_mul_f32 v[60:61], v[60:61], v[62:63]
	v_rcp_f32_e32 v62, v53
	v_fma_f32 v53, |v57|, s25, 1.0
	v_max_f32_e32 v58, 0, v58
	v_max_f32_e32 v59, 0, v59
	v_rcp_f32_e32 v63, v53
	v_pk_fma_f32 v[58:59], v[64:65], v[60:61], v[58:59] neg_lo:[1,0,0] neg_hi:[1,0,0]
	v_pk_mul_f32 v[64:65], v[56:57], v[56:57]
	v_readlane_b32 s0, v52, 7
	v_mul_f32_e32 v53, 0xbf38aa3b, v64
	v_exp_f32_e32 v64, v53
	v_mul_f32_e32 v53, 0xbf38aa3b, v65
	v_pk_fma_f32 v[66:67], v[62:63], s[22:23], v[90:91] op_sel_hi:[1,0,0]
	v_exp_f32_e32 v65, v53
	v_pk_mul_f32 v[52:53], s[0:1], v[54:55] op_sel_hi:[0,1]
	v_pk_fma_f32 v[66:67], v[62:63], v[66:67], s[24:25] op_sel_hi:[1,1,0]
	v_pk_fma_f32 v[42:43], v[52:53], v[238:239], v[242:243]
	v_pk_fma_f32 v[66:67], v[62:63], v[66:67], s[34:35] op_sel_hi:[1,1,0]
	v_fma_f32 v52, |v42|, s25, 1.0
	v_fma_f32 v53, |v43|, s25, 1.0
	v_pk_fma_f32 v[66:67], v[62:63], v[66:67], s[40:41] op_sel_hi:[1,1,0]
	v_rcp_f32_e32 v52, v52
	v_rcp_f32_e32 v53, v53
	v_and_b32_e32 v61, 0x7fffffff, v57
	v_and_b32_e32 v60, 0x7fffffff, v56
	v_pk_mul_f32 v[62:63], v[62:63], v[66:67]
	v_max_f32_e32 v56, 0, v56
	v_max_f32_e32 v57, 0, v57
	v_pk_mul_f32 v[60:61], v[60:61], v[62:63]
	v_cvt_pk_f16_f32 v58, v58, v59
	v_pk_fma_f32 v[56:57], v[64:65], v[60:61], v[56:57] neg_lo:[1,0,0] neg_hi:[1,0,0]
	v_pk_mul_f32 v[54:55], v[42:43], v[42:43]
	v_cvt_pk_f16_f32 v59, v56, v57
	v_pk_fma_f32 v[56:57], v[52:53], s[22:23], v[90:91] op_sel_hi:[1,0,0]
	v_mul_f32_e32 v54, 0xbf38aa3b, v54
	v_pk_fma_f32 v[56:57], v[52:53], v[56:57], s[24:25] op_sel_hi:[1,1,0]
	v_mul_f32_e32 v55, 0xbf38aa3b, v55
	v_exp_f32_e32 v54, v54
	v_pk_fma_f32 v[56:57], v[52:53], v[56:57], s[34:35] op_sel_hi:[1,1,0]
	v_exp_f32_e32 v55, v55
	v_pk_fma_f32 v[56:57], v[52:53], v[56:57], s[40:41] op_sel_hi:[1,1,0]
	v_and_b32_e32 v47, 0x7fffffff, v43
	v_and_b32_e32 v46, 0x7fffffff, v42
	v_pk_mul_f32 v[52:53], v[52:53], v[56:57]
	v_max_f32_e32 v42, 0, v42
	v_max_f32_e32 v43, 0, v43
	v_pk_mul_f32 v[46:47], v[46:47], v[52:53]
	ds_write_b64 v119, v[58:59] offset:39936
	v_pk_fma_f32 v[42:43], v[54:55], v[46:47], v[42:43] neg_lo:[1,0,0] neg_hi:[1,0,0]
	v_pk_mul_f32 v[46:47], s[0:1], v[50:51] op_sel_hi:[0,1]
	v_pk_fma_f32 v[44:45], v[46:47], v[240:241], v[244:245]
	v_cvt_pk_f16_f32 v42, v42, v43
	v_fma_f32 v43, |v44|, s25, 1.0
	v_rcp_f32_e32 v48, v43
	v_fma_f32 v43, |v45|, s25, 1.0
	v_rcp_f32_e32 v49, v43
	v_pk_mul_f32 v[50:51], v[44:45], v[44:45]
	v_and_b32_e32 v47, 0x7fffffff, v45
	v_mul_f32_e32 v43, 0xbf38aa3b, v50
	v_pk_fma_f32 v[52:53], v[48:49], s[22:23], v[90:91] op_sel_hi:[1,0,0]
	v_exp_f32_e32 v50, v43
	v_pk_fma_f32 v[52:53], v[48:49], v[52:53], s[24:25] op_sel_hi:[1,1,0]
	v_mul_f32_e32 v43, 0xbf38aa3b, v51
	v_pk_fma_f32 v[52:53], v[48:49], v[52:53], s[34:35] op_sel_hi:[1,1,0]
	v_exp_f32_e32 v51, v43
	v_pk_fma_f32 v[52:53], v[48:49], v[52:53], s[40:41] op_sel_hi:[1,1,0]
	v_and_b32_e32 v46, 0x7fffffff, v44
	v_pk_mul_f32 v[48:49], v[48:49], v[52:53]
	v_max_f32_e32 v44, 0, v44
	v_max_f32_e32 v45, 0, v45
	v_pk_mul_f32 v[46:47], v[46:47], v[48:49]
	s_waitcnt lgkmcnt(14)
	v_dot2c_f32_f16_e32 v104, v10, v10
	v_pk_fma_f32 v[44:45], v[50:51], v[46:47], v[44:45] neg_lo:[1,0,0] neg_hi:[1,0,0]
	v_dot2c_f32_f16_e32 v104, v11, v11
	v_cvt_pk_f16_f32 v43, v44, v45
	ds_write_b64 v146, v[42:43] offset:40448
	ds_read_b128 v[70:73], v115 offset:32768
	ds_read_b128 v[66:69], v147 offset:32768
	ds_read_b128 v[62:65], v148 offset:32768
	ds_read_b128 v[58:61], v149 offset:32768
	ds_read_b128 v[54:57], v150 offset:33024
	ds_read_b128 v[50:53], v151 offset:33024
	ds_read_b128 v[46:49], v152 offset:33024
	ds_read_b128 v[42:45], v153 offset:33024
	ds_read_b128 v[74:77], v95
	ds_read_b128 v[78:81], v95 offset:64
	ds_read_b128 v[82:85], v95 offset:128
	ds_read_b128 v[86:89], v95 offset:192
	ds_read_b128 v[90:93], v95 offset:256
	ds_read_b128 v[96:99], v95 offset:320
	s_waitcnt lgkmcnt(5)
	v_dot2c_f32_f16_e32 v105, v38, v74
	v_dot2c_f32_f16_e32 v105, v39, v75
	ds_read_b128 v[100:103], v95 offset:384
	ds_read_b128 v[108:111], v95 offset:448
	v_mov_b32_e32 v95, 0
	v_dot2c_f32_f16_e32 v105, v40, v76
	v_dot2c_f32_f16_e32 v95, v70, v70
	v_dot2c_f32_f16_e32 v105, v41, v77
	v_mov_b32_e32 v115, 0
	v_dot2c_f32_f16_e32 v95, v71, v71
	s_waitcnt lgkmcnt(6)
	v_dot2c_f32_f16_e32 v105, v34, v78
	v_dot2c_f32_f16_e32 v115, v70, v74
	v_dot2c_f32_f16_e32 v95, v72, v72
	v_dot2c_f32_f16_e32 v105, v35, v79
	v_dot2c_f32_f16_e32 v115, v71, v75
	v_dot2c_f32_f16_e32 v95, v73, v73
	v_dot2c_f32_f16_e32 v105, v36, v80
	v_dot2c_f32_f16_e32 v115, v72, v76
	v_dot2c_f32_f16_e32 v95, v66, v66
	v_dot2c_f32_f16_e32 v105, v37, v81
	v_dot2c_f32_f16_e32 v115, v73, v77
	v_dot2c_f32_f16_e32 v95, v67, v67
	s_waitcnt lgkmcnt(5)
	v_dot2c_f32_f16_e32 v105, v30, v82
	v_dot2c_f32_f16_e32 v115, v66, v78
	v_dot2c_f32_f16_e32 v95, v68, v68
	v_dot2c_f32_f16_e32 v105, v31, v83
	v_dot2c_f32_f16_e32 v115, v67, v79
	v_dot2c_f32_f16_e32 v95, v69, v69
	v_dot2c_f32_f16_e32 v105, v32, v84
	v_dot2c_f32_f16_e32 v115, v68, v80
	v_dot2c_f32_f16_e32 v95, v62, v62
	v_dot2c_f32_f16_e32 v105, v33, v85
	v_dot2c_f32_f16_e32 v115, v69, v81
	v_dot2c_f32_f16_e32 v95, v63, v63
	s_waitcnt lgkmcnt(4)
	v_dot2c_f32_f16_e32 v105, v26, v86
	v_dot2c_f32_f16_e32 v115, v62, v82
	v_dot2c_f32_f16_e32 v95, v64, v64
	v_dot2c_f32_f16_e32 v105, v27, v87
	v_dot2c_f32_f16_e32 v115, v63, v83
	v_dot2c_f32_f16_e32 v95, v65, v65
	v_dot2c_f32_f16_e32 v105, v28, v88
	v_dot2c_f32_f16_e32 v115, v64, v84
	v_dot2c_f32_f16_e32 v95, v58, v58
	v_dot2c_f32_f16_e32 v105, v29, v89
	v_dot2c_f32_f16_e32 v115, v65, v85
	v_dot2c_f32_f16_e32 v95, v59, v59
	s_waitcnt lgkmcnt(3)
	v_dot2c_f32_f16_e32 v105, v22, v90
	v_dot2c_f32_f16_e32 v115, v58, v86
	v_dot2c_f32_f16_e32 v95, v60, v60
	v_dot2c_f32_f16_e32 v105, v23, v91
	v_dot2c_f32_f16_e32 v115, v59, v87
	v_dot2c_f32_f16_e32 v95, v61, v61
	v_dot2c_f32_f16_e32 v105, v24, v92
	v_dot2c_f32_f16_e32 v115, v60, v88
	v_dot2c_f32_f16_e32 v95, v54, v54
	v_dot2c_f32_f16_e32 v105, v25, v93
	v_dot2c_f32_f16_e32 v115, v61, v89
	v_dot2c_f32_f16_e32 v95, v55, v55
	s_waitcnt lgkmcnt(2)
	v_dot2c_f32_f16_e32 v105, v18, v96
	v_dot2c_f32_f16_e32 v115, v54, v90
	v_dot2c_f32_f16_e32 v95, v56, v56
	v_dot2c_f32_f16_e32 v105, v19, v97
	v_dot2c_f32_f16_e32 v115, v55, v91
	v_dot2c_f32_f16_e32 v95, v57, v57
	v_dot2c_f32_f16_e32 v105, v20, v98
	v_dot2c_f32_f16_e32 v115, v56, v92
	v_dot2c_f32_f16_e32 v95, v50, v50
	v_dot2c_f32_f16_e32 v105, v21, v99
	v_dot2c_f32_f16_e32 v115, v57, v93
	v_dot2c_f32_f16_e32 v95, v51, v51
	s_waitcnt lgkmcnt(1)
	v_dot2c_f32_f16_e32 v105, v14, v100
	v_dot2c_f32_f16_e32 v115, v50, v96
	v_dot2c_f32_f16_e32 v95, v52, v52
	v_dot2c_f32_f16_e32 v105, v15, v101
	v_dot2c_f32_f16_e32 v115, v51, v97
	v_dot2c_f32_f16_e32 v95, v53, v53
	v_dot2c_f32_f16_e32 v105, v16, v102
	v_dot2c_f32_f16_e32 v115, v52, v98
	v_dot2c_f32_f16_e32 v95, v46, v46
	v_dot2c_f32_f16_e32 v105, v17, v103
	v_dot2c_f32_f16_e32 v115, v53, v99
	v_dot2c_f32_f16_e32 v95, v47, v47
	s_waitcnt lgkmcnt(0)
	v_dot2c_f32_f16_e32 v105, v10, v108
	v_dot2c_f32_f16_e32 v104, v12, v12
	v_dot2c_f32_f16_e32 v115, v46, v100
	v_dot2c_f32_f16_e32 v95, v48, v48
	v_dot2c_f32_f16_e32 v105, v11, v109
	v_dot2c_f32_f16_e32 v104, v13, v13
	v_dot2c_f32_f16_e32 v115, v47, v101
	v_dot2c_f32_f16_e32 v95, v49, v49
	v_dot2c_f32_f16_e32 v105, v12, v110
	v_dot2c_f32_f16_e32 v115, v48, v102
	v_dot2c_f32_f16_e32 v95, v42, v42
	v_mov_b32_e32 v74, v104
	v_dot2c_f32_f16_e32 v105, v13, v111
	v_dot2c_f32_f16_e32 v115, v49, v103
	v_dot2c_f32_f16_e32 v95, v43, v43
	v_permlane16_swap_b32_e32 v104, v74
	v_dot2c_f32_f16_e32 v115, v42, v108
	v_dot2c_f32_f16_e32 v95, v44, v44
	v_add_f32_e32 v133, v104, v74
	v_mov_b32_e32 v74, v105
	v_dot2c_f32_f16_e32 v115, v43, v109
	v_dot2c_f32_f16_e32 v95, v45, v45
	v_permlane16_swap_b32_e32 v105, v74
	v_dot2c_f32_f16_e32 v115, v44, v110
	v_add_f32_e32 v137, v105, v74
	v_mov_b32_e32 v74, v95
	v_dot2c_f32_f16_e32 v115, v45, v111
	s_nop 0
	v_permlane16_swap_b32_e32 v95, v74
	v_add_f32_e32 v135, v95, v74
	v_mov_b32_e32 v74, v115
	s_nop 1
	v_permlane16_swap_b32_e32 v115, v74
	v_add_f32_e32 v139, v115, v74
	v_lshlrev_b32_e32 v74, 8, v107
	v_lshlrev_b32_e32 v75, 3, v114
	s_movk_i32 s0, 0x78
	v_and_or_b32 v76, v75, s0, v74
	v_lshlrev_b32_e32 v75, 3, v141
	v_and_or_b32 v77, v75, s0, v74
	v_lshlrev_b32_e32 v75, 3, v142
	v_and_or_b32 v78, v75, s0, v74
	v_lshlrev_b32_e32 v75, 3, v143
	v_and_or_b32 v79, v75, s0, v74
	s_add_u32 s0, s26, 0x8000
	v_or_b32_e32 v108, 0x8000, v112
	v_mov_b32_e32 v123, 0
	s_addc_u32 s1, s27, 0
	v_readfirstlane_b32 s4, v108
	s_waitcnt vmcnt(0)
	s_barrier
	v_lshl_add_u64 v[74:75], s[0:1], 0, v[122:123]
	s_mov_b32 m0, s4
	s_nop 0
	global_load_lds_dwordx4 v[74:75], off
	s_addk_i32 s4, 0x400
	v_mov_b32_e32 v107, v123
	v_lshl_add_u64 v[74:75], s[0:1], 0, v[106:107]
	s_add_u32 s0, s26, 0xc000
	s_mov_b32 m0, s4
	s_nop 0
	global_load_lds_dwordx4 v[74:75], off
	s_addc_u32 s1, s27, 0
	v_or_b32_e32 v109, 0xc000, v112
	v_lshl_add_u64 v[74:75], s[0:1], 0, v[122:123]
	v_readfirstlane_b32 s4, v109
	s_mov_b32 m0, s4
	s_nop 0
	global_load_lds_dwordx4 v[74:75], off
	s_addk_i32 s4, 0x400
	v_lshl_add_u64 v[74:75], s[0:1], 0, v[106:107]
	s_mov_b32 m0, s4
	s_nop 0
	global_load_lds_dwordx4 v[74:75], off
	v_mov_b32_e32 v134, v133
	v_mov_b32_e32 v138, v137
	v_mov_b32_e32 v136, v135
	v_mov_b32_e32 v140, v139
	v_lshlrev_b32_e32 v144, 1, v76
	v_lshlrev_b32_e32 v143, 1, v77
	v_lshlrev_b32_e32 v142, 1, v78
	v_lshlrev_b32_e32 v141, 1, v79
	s_add_u32 s0, s26, 0x14000
	v_mov_b32_e32 v74, 0x7f61b1e6
	v_permlane32_swap_b32_e32 v133, v134
	v_permlane32_swap_b32_e32 v137, v138
	v_permlane32_swap_b32_e32 v135, v136
	v_permlane32_swap_b32_e32 v139, v140
	v_or_b32_e32 v160, 0x10000, v144
	v_or_b32_e32 v158, 0x10000, v143
	v_or_b32_e32 v156, 0x10000, v142
	v_or_b32_e32 v154, 0x10000, v141
	v_or_b32_e32 v159, 0x12000, v144
	v_or_b32_e32 v157, 0x12000, v143
	v_or_b32_e32 v155, 0x12000, v142
	v_or_b32_e32 v153, 0x12000, v141
	v_or_b32_e32 v152, 0x14000, v144
	v_or_b32_e32 v150, 0x14000, v143
	v_or_b32_e32 v148, 0x14000, v142
	v_or_b32_e32 v146, 0x14000, v141
	v_or_b32_e32 v151, 0x16000, v144
	v_or_b32_e32 v149, 0x16000, v143
	v_or_b32_e32 v147, 0x16000, v142
	v_or_b32_e32 v145, 0x16000, v141
	s_addc_u32 s1, s27, 0
	v_mov_b32_e32 v98, 0x7f800000
	s_mov_b32 s22, 0
	v_mov_b32_e32 v100, 0x7f800000
	v_mov_b32_e32 v99, 0x7f800000
	v_mov_b32_e32 v111, 0x7f800000
	v_mov_b32_e32 v101, 0x7f800000
	v_mov_b32_e32 v110, 0x7f800000
	v_mov_b32_e32 v75, v74
	v_mov_b32_e32 v76, v74
	v_mov_b32_e32 v77, v74
	v_mov_b32_e32 v78, v74
	v_mov_b32_e32 v79, v74
	v_mov_b32_e32 v80, v74
	v_mov_b32_e32 v81, v74
	v_mov_b32_e32 v82, v74
	v_mov_b32_e32 v83, v74
	v_mov_b32_e32 v84, v74
	v_mov_b32_e32 v85, v74
	v_mov_b32_e32 v86, v74
	v_mov_b32_e32 v87, v74
	v_mov_b32_e32 v88, v74
	v_mov_b32_e32 v89, v74
	v_mov_b32_e32 v247, 0xfffffc00
	v_readfirstlane_b32 s96, v1
	s_nop 3
	s_cmp_lt_u32 s96, 4
	s_cbranch_scc0 .Lmy_prio_done
	s_setprio 1
